# RG-LRU: gate-stage X fragments read from LDS up front with counted waits, store-drain waits removed from chunk loop; grid barrier one-hop; on top of carry-ladder rewrite
# speedup vs baseline: 1.0035x; 1.0035x over previous
; __device__ __forceinline__ void unit(LAS unsigned char* lds, const bf16* __restrict__ xr, const bf16* __restrict__ yg, const float* __restrict__ conv_w, const float* __restrict__ conv_b, const bf16* __restrict__ wga_t, const bf16* __restrict__ wgx_t, ...
;     ...
;     for (int dt = 0; dt < 2; ++dt)
; #pragma unroll
;         for (int r = 0; r < 4; ++r) { const int c = n * 128 + hf * 64 + dq * 32 + 16 * dt + 4 * l4 + r; cba[dt][r] = b_ga[c]; cbx[dt][r] = b_gx[c]; csp[dt][r] = -8.0f * log1pf(__expf(-lam[c])); }
.LBB5_935:
	s_waitcnt vmcnt(0)
	v_mul_f32_e32 v86, 0xbfb8aa3b, v86
	v_exp_f32_e32 v86, v86
	v_mul_f32_e32 v87, 0xbfb8aa3b, v87
	v_mul_f32_e32 v82, 0xbfb8aa3b, v82
	v_exp_f32_e32 v82, v82
	v_add_f32_e32 v94, 1.0, v86
	v_add_f32_e32 v92, -1.0, v94
	v_sub_f32_e32 v93, v92, v94
	v_sub_f32_e32 v92, v86, v92
	v_add_f32_e32 v93, 1.0, v93
	v_frexp_mant_f32_e32 v95, v94
	v_add_f32_e32 v96, v92, v93
	v_cvt_f64_f32_e32 v[92:93], v94
	v_frexp_exp_i32_f64_e32 v92, v[92:93]
	v_cmp_gt_f32_e32 vcc, s74, v95
	v_mul_f32_e32 v83, 0xbfb8aa3b, v83
	s_and_b32 s42, s79, 1
	v_subbrev_co_u32_e32 v92, vcc, 0, v92, vcc
	v_sub_u32_e32 v93, 0, v92
	v_ldexp_f32 v94, v94, v93
	v_add_f32_e32 v95, -1.0, v94
	v_add_f32_e32 v107, 1.0, v94
	v_ldexp_f32 v93, v96, v93
	v_add_f32_e32 v96, 1.0, v95
	v_add_f32_e32 v118, -1.0, v107
	v_sub_f32_e32 v96, v94, v96
	v_sub_f32_e32 v94, v94, v118
	v_add_f32_e32 v96, v93, v96
	v_add_f32_e32 v93, v93, v94
	v_add_f32_e32 v94, v107, v93
	v_rcp_f32_e32 v118, v94
	v_add_f32_e32 v97, v95, v96
	v_sub_f32_e32 v95, v97, v95
	v_sub_f32_e32 v95, v96, v95
	v_sub_f32_e32 v96, v94, v107
	v_sub_f32_e32 v93, v93, v96
	v_mul_f32_e32 v96, v97, v118
	v_mul_f32_e32 v107, v94, v96
	v_fma_f32 v119, v96, v94, -v107
	v_fmac_f32_e32 v119, v96, v93
	v_add_f32_e32 v120, v107, v119
	v_sub_f32_e32 v121, v97, v120
	v_sub_f32_e32 v97, v97, v121
	v_sub_f32_e32 v107, v120, v107
	v_sub_f32_e32 v97, v97, v120
	v_add_f32_e32 v95, v95, v97
	v_sub_f32_e32 v97, v107, v119
	v_add_f32_e32 v95, v97, v95
	v_add_f32_e32 v97, v121, v95
	v_mul_f32_e32 v107, v118, v97
	v_mul_f32_e32 v119, v94, v107
	v_fma_f32 v94, v107, v94, -v119
	v_fmac_f32_e32 v94, v107, v93
	v_sub_f32_e32 v93, v121, v97
	v_add_f32_e32 v93, v95, v93
	v_add_f32_e32 v95, v119, v94
	v_sub_f32_e32 v120, v97, v95
	v_sub_f32_e32 v97, v97, v120
	v_sub_f32_e32 v119, v95, v119
	v_sub_f32_e32 v95, v97, v95
	v_add_f32_e32 v93, v93, v95
	v_sub_f32_e32 v94, v119, v94
	v_cvt_f32_i32_e32 v92, v92
	v_add_f32_e32 v93, v94, v93
	v_add_f32_e32 v94, v96, v107
	v_add_f32_e32 v93, v120, v93
	v_sub_f32_e32 v95, v94, v96
	v_mul_f32_e32 v93, v118, v93
	v_sub_f32_e32 v95, v107, v95
	v_add_f32_e32 v93, v95, v93
	v_mul_f32_e32 v107, 0x3f317218, v92
	v_add_f32_e32 v95, v94, v93
	v_fma_f32 v118, v92, s75, -v107
	v_mul_f32_e32 v96, v95, v95
	v_fmac_f32_e32 v118, 0xb102e308, v92
	v_sub_f32_e32 v92, v95, v94
	v_fmamk_f32 v97, v96, 0x3e9b6dac, v133
	v_sub_f32_e32 v92, v93, v92
	v_add_f32_e32 v93, v107, v118
	v_fmaak_f32 v97, v96, v97, 0x3f2aaada
	v_sub_f32_e32 v94, v93, v107
	v_ldexp_f32 v107, v95, 1
	v_mul_f32_e32 v95, v95, v96
	v_mul_f32_e32 v95, v95, v97
	v_add_f32_e32 v96, v107, v95
	v_sub_f32_e32 v97, v96, v107
	v_ldexp_f32 v92, v92, 1
	v_sub_f32_e32 v95, v95, v97
	v_add_f32_e32 v92, v92, v95
	v_add_f32_e32 v95, v96, v92
	v_sub_f32_e32 v96, v95, v96
	v_sub_f32_e32 v92, v92, v96
	v_add_f32_e32 v96, v93, v95
	v_sub_f32_e32 v97, v96, v93
	v_sub_f32_e32 v107, v96, v97
	v_sub_f32_e32 v94, v118, v94
	v_sub_f32_e32 v93, v93, v107
	v_sub_f32_e32 v95, v95, v97
	v_add_f32_e32 v93, v95, v93
	v_add_f32_e32 v95, v94, v92
	v_sub_f32_e32 v97, v95, v94
	v_sub_f32_e32 v107, v95, v97
	v_sub_f32_e32 v94, v94, v107
	v_sub_f32_e32 v92, v92, v97
	v_add_f32_e32 v93, v95, v93
	v_add_f32_e32 v92, v92, v94
	v_add_f32_e32 v94, v96, v93
	v_sub_f32_e32 v95, v94, v96
	v_sub_f32_e32 v93, v93, v95
	v_add_f32_e32 v92, v92, v93
	v_add_f32_e32 v92, v94, v92
	v_cmp_neq_f32_e32 vcc, s76, v86
	v_exp_f32_e32 v93, v87
	s_lshl_b64 s[6:7], s[6:7], 1
	v_cndmask_b32_e32 v92, v134, v92, vcc
	v_cmp_ngt_f32_e32 vcc, -1.0, v86
	s_add_u32 s6, s17, s6
	s_addc_u32 s7, s27, s7
	v_cndmask_b32_e32 v92, v135, v92, vcc
	v_cmp_neq_f32_e32 vcc, -1.0, v86
	s_lshl_b32 s43, s78, 7
	s_and_b32 s89, s43, 0x700
	v_cndmask_b32_e32 v92, v136, v92, vcc
	v_cmp_lt_f32_e64 vcc, |v86|, s77
	s_and_b32 s43, s78, 15
	s_lshl_b32 s92, s43, 2
	v_cndmask_b32_e32 v86, v92, v86, vcc
	v_add_f32_e32 v92, 1.0, v93
	v_mul_f32_e32 v139, 0xc1000000, v86
	v_add_f32_e32 v86, -1.0, v92
	v_sub_f32_e32 v87, v86, v92
	v_add_f32_e32 v87, 1.0, v87
	v_sub_f32_e32 v86, v93, v86
	v_add_f32_e32 v94, v86, v87
	v_frexp_mant_f32_e32 v95, v92
	v_cvt_f64_f32_e32 v[86:87], v92
	v_frexp_exp_i32_f64_e32 v86, v[86:87]
	v_cmp_gt_f32_e32 vcc, s74, v95
	s_add_u32 s6, s6, s54
	s_addc_u32 s7, s7, 0
	v_subbrev_co_u32_e32 v86, vcc, 0, v86, vcc
	v_sub_u32_e32 v87, 0, v86
	v_ldexp_f32 v92, v92, v87
	v_ldexp_f32 v87, v94, v87
	v_add_f32_e32 v94, -1.0, v92
	v_add_f32_e32 v97, 1.0, v92
	v_add_f32_e32 v95, 1.0, v94
	v_add_f32_e32 v107, -1.0, v97
	v_sub_f32_e32 v95, v92, v95
	v_sub_f32_e32 v92, v92, v107
	v_add_f32_e32 v95, v87, v95
	v_add_f32_e32 v87, v87, v92
	v_add_f32_e32 v92, v97, v87
	v_rcp_f32_e32 v107, v92
	v_add_f32_e32 v96, v94, v95
	v_sub_f32_e32 v94, v96, v94
	v_sub_f32_e32 v94, v95, v94
	v_sub_f32_e32 v95, v92, v97
	v_sub_f32_e32 v87, v87, v95
	v_mul_f32_e32 v95, v96, v107
	v_mul_f32_e32 v97, v92, v95
	v_fma_f32 v118, v95, v92, -v97
	v_fmac_f32_e32 v118, v95, v87
	v_add_f32_e32 v119, v97, v118
	v_sub_f32_e32 v120, v96, v119
	v_sub_f32_e32 v96, v96, v120
	v_sub_f32_e32 v97, v119, v97
	v_sub_f32_e32 v96, v96, v119
	v_add_f32_e32 v94, v94, v96
	v_sub_f32_e32 v96, v97, v118
	v_add_f32_e32 v94, v96, v94
	v_add_f32_e32 v96, v120, v94
	v_mul_f32_e32 v97, v107, v96
	v_mul_f32_e32 v118, v92, v97
	v_fma_f32 v92, v97, v92, -v118
	v_fmac_f32_e32 v92, v97, v87
	v_sub_f32_e32 v87, v120, v96
	v_add_f32_e32 v87, v94, v87
	v_add_f32_e32 v94, v118, v92
	v_sub_f32_e32 v119, v96, v94
	v_sub_f32_e32 v96, v96, v119
	v_sub_f32_e32 v118, v94, v118
	v_sub_f32_e32 v94, v96, v94
	v_add_f32_e32 v87, v87, v94
	v_sub_f32_e32 v92, v118, v92
	v_cvt_f32_i32_e32 v86, v86
; __device__ __forceinline__ void unit(LAS unsigned char* lds, const bf16* __restrict__ xr, const bf16* __restrict__ yg, const float* __restrict__ conv_w, const float* __restrict__ conv_b, const bf16* __restrict__ wga_t, const bf16* __restrict__ wgx_t, ...
;     ...
;     for (int dt = 0; dt < 2; ++dt)
; #pragma unroll
;         for (int r = 0; r < 4; ++r) { const int c = n * 128 + hf * 64 + dq * 32 + 16 * dt + 4 * l4 + r; cba[dt][r] = b_ga[c]; cbx[dt][r] = b_gx[c]; csp[dt][r] = -8.0f * log1pf(__expf(-lam[c])); }
	v_add_f32_e32 v87, v92, v87
	v_add_f32_e32 v92, v95, v97
	v_add_f32_e32 v87, v119, v87
	v_sub_f32_e32 v94, v92, v95
	v_mul_f32_e32 v87, v107, v87
	v_sub_f32_e32 v94, v97, v94
	v_add_f32_e32 v87, v94, v87
	v_mul_f32_e32 v97, 0x3f317218, v86
	v_add_f32_e32 v94, v92, v87
	v_fma_f32 v107, v86, s75, -v97
	v_mul_f32_e32 v95, v94, v94
	v_fmac_f32_e32 v107, 0xb102e308, v86
	v_sub_f32_e32 v86, v94, v92
	v_fmamk_f32 v96, v95, 0x3e9b6dac, v133
	v_sub_f32_e32 v86, v87, v86
	v_add_f32_e32 v87, v97, v107
	v_fmaak_f32 v96, v95, v96, 0x3f2aaada
	v_sub_f32_e32 v92, v87, v97
	v_ldexp_f32 v97, v94, 1
	v_mul_f32_e32 v94, v94, v95
	v_mul_f32_e32 v94, v94, v96
	v_add_f32_e32 v95, v97, v94
	v_sub_f32_e32 v96, v95, v97
	v_ldexp_f32 v86, v86, 1
	v_sub_f32_e32 v94, v94, v96
	v_add_f32_e32 v86, v86, v94
	v_add_f32_e32 v94, v95, v86
	v_sub_f32_e32 v95, v94, v95
	v_sub_f32_e32 v86, v86, v95
	v_add_f32_e32 v95, v87, v94
	v_sub_f32_e32 v96, v95, v87
	v_sub_f32_e32 v97, v95, v96
	v_sub_f32_e32 v92, v107, v92
	v_sub_f32_e32 v87, v87, v97
	v_sub_f32_e32 v94, v94, v96
	v_add_f32_e32 v87, v94, v87
	v_add_f32_e32 v94, v92, v86
	v_sub_f32_e32 v96, v94, v92
	v_sub_f32_e32 v97, v94, v96
	v_sub_f32_e32 v92, v92, v97
	v_sub_f32_e32 v86, v86, v96
	v_add_f32_e32 v87, v94, v87
	v_add_f32_e32 v86, v86, v92
	v_add_f32_e32 v92, v95, v87
	v_sub_f32_e32 v94, v92, v95
	v_sub_f32_e32 v87, v87, v94
	v_add_f32_e32 v86, v86, v87
	v_mul_f32_e32 v87, 0xbfb8aa3b, v88
	v_add_f32_e32 v86, v92, v86
	v_cmp_neq_f32_e32 vcc, s76, v93
	v_exp_f32_e32 v88, v87
	s_lshl_b32 s43, s42, 7
	v_cndmask_b32_e32 v86, v134, v86, vcc
	v_cmp_ngt_f32_e32 vcc, -1.0, v93
	v_add_f32_e32 v92, 1.0, v88
	v_frexp_mant_f32_e32 v94, v92
	v_cndmask_b32_e32 v86, v135, v86, vcc
	v_cmp_neq_f32_e32 vcc, -1.0, v93
	s_add_u32 s6, s6, s43
	s_addc_u32 s7, s7, 0
	v_cndmask_b32_e32 v86, v136, v86, vcc
	v_cmp_lt_f32_e64 vcc, |v93|, s77
	s_mul_i32 s50, s34, 0x880
	v_add_u32_e32 v156, s50, v126
	v_cndmask_b32_e32 v86, v86, v93, vcc
	v_mul_f32_e32 v140, 0xc1000000, v86
	v_add_f32_e32 v86, -1.0, v92
	v_sub_f32_e32 v87, v86, v92
	v_add_f32_e32 v87, 1.0, v87
	v_sub_f32_e32 v86, v88, v86
	v_add_f32_e32 v93, v86, v87
	v_cvt_f64_f32_e32 v[86:87], v92
	v_frexp_exp_i32_f64_e32 v86, v[86:87]
	v_cmp_gt_f32_e32 vcc, s74, v94
	s_nop 1
	v_subbrev_co_u32_e32 v86, vcc, 0, v86, vcc
	v_sub_u32_e32 v87, 0, v86
	v_ldexp_f32 v92, v92, v87
	v_ldexp_f32 v87, v93, v87
	v_add_f32_e32 v93, -1.0, v92
	v_add_f32_e32 v96, 1.0, v92
	v_add_f32_e32 v94, 1.0, v93
	v_add_f32_e32 v97, -1.0, v96
	v_sub_f32_e32 v94, v92, v94
	v_sub_f32_e32 v92, v92, v97
	v_add_f32_e32 v94, v87, v94
	v_add_f32_e32 v87, v87, v92
	v_add_f32_e32 v92, v96, v87
	v_rcp_f32_e32 v97, v92
	v_add_f32_e32 v95, v93, v94
	v_sub_f32_e32 v93, v95, v93
	v_sub_f32_e32 v93, v94, v93
	v_sub_f32_e32 v94, v92, v96
	v_sub_f32_e32 v87, v87, v94
	v_mul_f32_e32 v94, v95, v97
	v_mul_f32_e32 v96, v92, v94
	v_fma_f32 v107, v94, v92, -v96
	v_fmac_f32_e32 v107, v94, v87
	v_add_f32_e32 v118, v96, v107
	v_sub_f32_e32 v119, v95, v118
	v_sub_f32_e32 v95, v95, v119
	v_sub_f32_e32 v96, v118, v96
	v_sub_f32_e32 v95, v95, v118
	v_add_f32_e32 v93, v93, v95
	v_sub_f32_e32 v95, v96, v107
	v_add_f32_e32 v93, v95, v93
	v_add_f32_e32 v95, v119, v93
	v_mul_f32_e32 v96, v97, v95
	v_mul_f32_e32 v107, v92, v96
	v_fma_f32 v92, v96, v92, -v107
	v_fmac_f32_e32 v92, v96, v87
	v_sub_f32_e32 v87, v119, v95
	v_add_f32_e32 v87, v93, v87
	v_add_f32_e32 v93, v107, v92
	v_sub_f32_e32 v118, v95, v93
	v_sub_f32_e32 v95, v95, v118
	v_sub_f32_e32 v107, v93, v107
	v_sub_f32_e32 v93, v95, v93
	v_add_f32_e32 v87, v87, v93
	v_sub_f32_e32 v92, v107, v92
	v_cvt_f32_i32_e32 v86, v86
	v_add_f32_e32 v87, v92, v87
	v_add_f32_e32 v92, v94, v96
	v_add_f32_e32 v87, v118, v87
	v_sub_f32_e32 v93, v92, v94
	v_mul_f32_e32 v87, v97, v87
	v_sub_f32_e32 v93, v96, v93
	v_add_f32_e32 v87, v93, v87
	v_mul_f32_e32 v96, 0x3f317218, v86
	v_add_f32_e32 v93, v92, v87
	v_fma_f32 v97, v86, s75, -v96
	v_mul_f32_e32 v94, v93, v93
	v_fmac_f32_e32 v97, 0xb102e308, v86
	v_sub_f32_e32 v86, v93, v92
	v_fmamk_f32 v95, v94, 0x3e9b6dac, v133
	v_sub_f32_e32 v86, v87, v86
	v_add_f32_e32 v87, v96, v97
	v_fmaak_f32 v95, v94, v95, 0x3f2aaada
	v_sub_f32_e32 v92, v87, v96
	v_ldexp_f32 v96, v93, 1
	v_mul_f32_e32 v93, v93, v94
	v_mul_f32_e32 v93, v93, v95
	v_add_f32_e32 v94, v96, v93
	v_sub_f32_e32 v95, v94, v96
	v_ldexp_f32 v86, v86, 1
	v_sub_f32_e32 v93, v93, v95
	v_add_f32_e32 v86, v86, v93
	v_add_f32_e32 v93, v94, v86
	v_sub_f32_e32 v94, v93, v94
	v_sub_f32_e32 v86, v86, v94
	v_add_f32_e32 v94, v87, v93
	v_sub_f32_e32 v95, v94, v87
	v_sub_f32_e32 v96, v94, v95
	v_sub_f32_e32 v92, v97, v92
	v_sub_f32_e32 v87, v87, v96
	v_sub_f32_e32 v93, v93, v95
	v_add_f32_e32 v87, v93, v87
	v_add_f32_e32 v93, v92, v86
	v_sub_f32_e32 v95, v93, v92
	v_sub_f32_e32 v96, v93, v95
	v_sub_f32_e32 v92, v92, v96
	v_sub_f32_e32 v86, v86, v95
	v_add_f32_e32 v87, v93, v87
	v_add_f32_e32 v86, v86, v92
	v_add_f32_e32 v92, v94, v87
	v_sub_f32_e32 v93, v92, v94
	v_sub_f32_e32 v87, v87, v93
	v_add_f32_e32 v86, v86, v87
	v_mul_f32_e32 v87, 0xbfb8aa3b, v89
	v_add_f32_e32 v86, v92, v86
	v_cmp_neq_f32_e32 vcc, s76, v88
	v_exp_f32_e32 v89, v87
	s_nop 0
	v_cndmask_b32_e32 v86, v134, v86, vcc
	v_cmp_ngt_f32_e32 vcc, -1.0, v88
	s_nop 1
	v_cndmask_b32_e32 v86, v135, v86, vcc
	v_cmp_neq_f32_e32 vcc, -1.0, v88
	s_nop 1
	v_cndmask_b32_e32 v86, v136, v86, vcc
	v_cmp_lt_f32_e64 vcc, |v88|, s77
	s_nop 1
	v_cndmask_b32_e32 v86, v86, v88, vcc
	v_add_f32_e32 v88, 1.0, v89
	v_mul_f32_e32 v141, 0xc1000000, v86
	v_add_f32_e32 v86, -1.0, v88
	v_sub_f32_e32 v87, v86, v88
	v_add_f32_e32 v87, 1.0, v87
	v_sub_f32_e32 v86, v89, v86
	v_add_f32_e32 v92, v86, v87
; __device__ __forceinline__ void unit(LAS unsigned char* lds, const bf16* __restrict__ xr, const bf16* __restrict__ yg, const float* __restrict__ conv_w, const float* __restrict__ conv_b, const bf16* __restrict__ wga_t, const bf16* __restrict__ wgx_t, ...
;     ...
;     for (int dt = 0; dt < 2; ++dt)
; #pragma unroll
;         for (int r = 0; r < 4; ++r) { const int c = n * 128 + hf * 64 + dq * 32 + 16 * dt + 4 * l4 + r; cba[dt][r] = b_ga[c]; cbx[dt][r] = b_gx[c]; csp[dt][r] = -8.0f * log1pf(__expf(-lam[c])); }
	v_frexp_mant_f32_e32 v93, v88
	v_cvt_f64_f32_e32 v[86:87], v88
	v_frexp_exp_i32_f64_e32 v86, v[86:87]
	v_cmp_gt_f32_e32 vcc, s74, v93
	s_nop 1
	v_subbrev_co_u32_e32 v86, vcc, 0, v86, vcc
	v_sub_u32_e32 v87, 0, v86
	v_ldexp_f32 v88, v88, v87
	v_ldexp_f32 v87, v92, v87
	v_add_f32_e32 v92, -1.0, v88
	v_add_f32_e32 v95, 1.0, v88
	v_add_f32_e32 v93, 1.0, v92
	v_add_f32_e32 v96, -1.0, v95
	v_sub_f32_e32 v93, v88, v93
	v_sub_f32_e32 v88, v88, v96
	v_add_f32_e32 v93, v87, v93
	v_add_f32_e32 v87, v87, v88
	v_add_f32_e32 v88, v95, v87
	v_rcp_f32_e32 v96, v88
	v_add_f32_e32 v94, v92, v93
	v_sub_f32_e32 v92, v94, v92
	v_sub_f32_e32 v92, v93, v92
	v_sub_f32_e32 v93, v88, v95
	v_sub_f32_e32 v87, v87, v93
	v_mul_f32_e32 v93, v94, v96
	v_mul_f32_e32 v95, v88, v93
	v_fma_f32 v97, v93, v88, -v95
	v_fmac_f32_e32 v97, v93, v87
	v_add_f32_e32 v107, v95, v97
	v_sub_f32_e32 v118, v94, v107
	v_sub_f32_e32 v94, v94, v118
	v_sub_f32_e32 v95, v107, v95
	v_sub_f32_e32 v94, v94, v107
	v_add_f32_e32 v92, v92, v94
	v_sub_f32_e32 v94, v95, v97
	v_add_f32_e32 v92, v94, v92
	v_add_f32_e32 v94, v118, v92
	v_mul_f32_e32 v95, v96, v94
	v_mul_f32_e32 v97, v88, v95
	v_fma_f32 v88, v95, v88, -v97
	v_fmac_f32_e32 v88, v95, v87
	v_sub_f32_e32 v87, v118, v94
	v_add_f32_e32 v87, v92, v87
	v_add_f32_e32 v92, v97, v88
	v_sub_f32_e32 v107, v94, v92
	v_sub_f32_e32 v94, v94, v107
	v_sub_f32_e32 v97, v92, v97
	v_sub_f32_e32 v92, v94, v92
	v_add_f32_e32 v87, v87, v92
	v_sub_f32_e32 v88, v97, v88
	v_cvt_f32_i32_e32 v86, v86
	v_add_f32_e32 v87, v88, v87
	v_add_f32_e32 v88, v93, v95
	v_add_f32_e32 v87, v107, v87
	v_sub_f32_e32 v92, v88, v93
	v_mul_f32_e32 v87, v96, v87
	v_sub_f32_e32 v92, v95, v92
	v_add_f32_e32 v87, v92, v87
	v_mul_f32_e32 v95, 0x3f317218, v86
	v_add_f32_e32 v92, v88, v87
	v_fma_f32 v96, v86, s75, -v95
	v_mul_f32_e32 v93, v92, v92
	v_fmac_f32_e32 v96, 0xb102e308, v86
	v_sub_f32_e32 v86, v92, v88
	v_fmamk_f32 v94, v93, 0x3e9b6dac, v133
	v_sub_f32_e32 v86, v87, v86
	v_add_f32_e32 v87, v95, v96
	v_fmaak_f32 v94, v93, v94, 0x3f2aaada
	v_sub_f32_e32 v88, v87, v95
	v_ldexp_f32 v95, v92, 1
	v_mul_f32_e32 v92, v92, v93
	v_mul_f32_e32 v92, v92, v94
	v_add_f32_e32 v93, v95, v92
	v_sub_f32_e32 v94, v93, v95
	v_ldexp_f32 v86, v86, 1
	v_sub_f32_e32 v92, v92, v94
	v_add_f32_e32 v86, v86, v92
	v_add_f32_e32 v92, v93, v86
	v_sub_f32_e32 v93, v92, v93
	v_sub_f32_e32 v86, v86, v93
	v_add_f32_e32 v93, v87, v92
	v_sub_f32_e32 v94, v93, v87
	v_sub_f32_e32 v95, v93, v94
	v_sub_f32_e32 v88, v96, v88
	v_sub_f32_e32 v87, v87, v95
	v_sub_f32_e32 v92, v92, v94
	v_add_f32_e32 v87, v92, v87
	v_add_f32_e32 v92, v88, v86
	v_sub_f32_e32 v94, v92, v88
	v_sub_f32_e32 v95, v92, v94
	v_sub_f32_e32 v88, v88, v95
	v_sub_f32_e32 v86, v86, v94
	v_add_f32_e32 v87, v92, v87
	v_add_f32_e32 v86, v86, v88
	v_add_f32_e32 v88, v93, v87
	v_sub_f32_e32 v92, v88, v93
	v_sub_f32_e32 v87, v87, v92
	v_add_f32_e32 v86, v86, v87
	v_add_f32_e32 v86, v88, v86
	v_cmp_neq_f32_e32 vcc, s76, v89
	v_add_f32_e32 v88, 1.0, v82
	v_frexp_mant_f32_e32 v92, v88
	v_cndmask_b32_e32 v86, v134, v86, vcc
	v_cmp_ngt_f32_e32 vcc, -1.0, v89
	s_nop 1
	v_cndmask_b32_e32 v86, v135, v86, vcc
	v_cmp_neq_f32_e32 vcc, -1.0, v89
	s_nop 1
	v_cndmask_b32_e32 v86, v136, v86, vcc
	v_cmp_lt_f32_e64 vcc, |v89|, s77
	s_nop 1
	v_cndmask_b32_e32 v86, v86, v89, vcc
	v_mul_f32_e32 v142, 0xc1000000, v86
	v_add_f32_e32 v86, -1.0, v88
	v_sub_f32_e32 v87, v86, v88
	v_add_f32_e32 v87, 1.0, v87
	v_sub_f32_e32 v86, v82, v86
	v_add_f32_e32 v89, v86, v87
	v_cvt_f64_f32_e32 v[86:87], v88
	v_frexp_exp_i32_f64_e32 v86, v[86:87]
	v_cmp_gt_f32_e32 vcc, s74, v92
	s_nop 1
	v_subbrev_co_u32_e32 v86, vcc, 0, v86, vcc
	v_sub_u32_e32 v87, 0, v86
	v_ldexp_f32 v88, v88, v87
	v_ldexp_f32 v87, v89, v87
	v_add_f32_e32 v89, -1.0, v88
	v_add_f32_e32 v94, 1.0, v88
	v_add_f32_e32 v92, 1.0, v89
	v_add_f32_e32 v95, -1.0, v94
	v_sub_f32_e32 v92, v88, v92
	v_sub_f32_e32 v88, v88, v95
	v_add_f32_e32 v92, v87, v92
	v_add_f32_e32 v87, v87, v88
	v_add_f32_e32 v88, v94, v87
	v_rcp_f32_e32 v95, v88
	v_add_f32_e32 v93, v89, v92
	v_sub_f32_e32 v89, v93, v89
	v_sub_f32_e32 v89, v92, v89
	v_sub_f32_e32 v92, v88, v94
	v_sub_f32_e32 v87, v87, v92
	v_mul_f32_e32 v92, v93, v95
	v_mul_f32_e32 v94, v88, v92
	v_fma_f32 v96, v92, v88, -v94
	v_fmac_f32_e32 v96, v92, v87
	v_add_f32_e32 v97, v94, v96
	v_sub_f32_e32 v107, v93, v97
	v_sub_f32_e32 v93, v93, v107
	v_sub_f32_e32 v94, v97, v94
	v_sub_f32_e32 v93, v93, v97
	v_add_f32_e32 v89, v89, v93
	v_sub_f32_e32 v93, v94, v96
	v_add_f32_e32 v89, v93, v89
	v_add_f32_e32 v93, v107, v89
	v_mul_f32_e32 v94, v95, v93
	v_mul_f32_e32 v96, v88, v94
	v_fma_f32 v88, v94, v88, -v96
	v_fmac_f32_e32 v88, v94, v87
	v_sub_f32_e32 v87, v107, v93
	v_add_f32_e32 v87, v89, v87
	v_add_f32_e32 v89, v96, v88
	v_sub_f32_e32 v97, v93, v89
	v_sub_f32_e32 v93, v93, v97
	v_sub_f32_e32 v96, v89, v96
	v_sub_f32_e32 v89, v93, v89
	v_add_f32_e32 v87, v87, v89
	v_sub_f32_e32 v88, v96, v88
	v_cvt_f32_i32_e32 v86, v86
	v_add_f32_e32 v87, v88, v87
	v_add_f32_e32 v88, v92, v94
	v_add_f32_e32 v87, v97, v87
	v_sub_f32_e32 v89, v88, v92
	v_mul_f32_e32 v87, v95, v87
	v_sub_f32_e32 v89, v94, v89
	v_add_f32_e32 v87, v89, v87
	v_mul_f32_e32 v94, 0x3f317218, v86
	v_add_f32_e32 v89, v88, v87
	v_fma_f32 v95, v86, s75, -v94
	v_mul_f32_e32 v92, v89, v89
	v_fmac_f32_e32 v95, 0xb102e308, v86
	v_sub_f32_e32 v86, v89, v88
	v_fmamk_f32 v93, v92, 0x3e9b6dac, v133
	v_sub_f32_e32 v86, v87, v86
	v_add_f32_e32 v87, v94, v95
	v_fmaak_f32 v93, v92, v93, 0x3f2aaada
	v_sub_f32_e32 v88, v87, v94
	v_ldexp_f32 v94, v89, 1
	v_mul_f32_e32 v89, v89, v92
	v_mul_f32_e32 v89, v89, v93
	v_add_f32_e32 v92, v94, v89
	v_sub_f32_e32 v93, v92, v94
; __device__ __forceinline__ void unit(LAS unsigned char* lds, const bf16* __restrict__ xr, const bf16* __restrict__ yg, const float* __restrict__ conv_w, const float* __restrict__ conv_b, const bf16* __restrict__ wga_t, const bf16* __restrict__ wgx_t, ...
;     ...
;     for (int dt = 0; dt < 2; ++dt)
; #pragma unroll
;         for (int r = 0; r < 4; ++r) { const int c = n * 128 + hf * 64 + dq * 32 + 16 * dt + 4 * l4 + r; cba[dt][r] = b_ga[c]; cbx[dt][r] = b_gx[c]; csp[dt][r] = -8.0f * log1pf(__expf(-lam[c])); }
	v_ldexp_f32 v86, v86, 1
	v_sub_f32_e32 v89, v89, v93
	v_add_f32_e32 v86, v86, v89
	v_add_f32_e32 v89, v92, v86
	v_sub_f32_e32 v92, v89, v92
	v_sub_f32_e32 v86, v86, v92
	v_add_f32_e32 v92, v87, v89
	v_sub_f32_e32 v93, v92, v87
	v_sub_f32_e32 v94, v92, v93
	v_sub_f32_e32 v88, v95, v88
	v_sub_f32_e32 v87, v87, v94
	v_sub_f32_e32 v89, v89, v93
	v_add_f32_e32 v87, v89, v87
	v_add_f32_e32 v89, v88, v86
	v_sub_f32_e32 v93, v89, v88
	v_sub_f32_e32 v94, v89, v93
	v_sub_f32_e32 v88, v88, v94
	v_sub_f32_e32 v86, v86, v93
	v_add_f32_e32 v87, v89, v87
	v_add_f32_e32 v86, v86, v88
	v_add_f32_e32 v88, v92, v87
	v_sub_f32_e32 v89, v88, v92
	v_sub_f32_e32 v87, v87, v89
	v_add_f32_e32 v86, v86, v87
	v_add_f32_e32 v86, v88, v86
	v_cmp_neq_f32_e32 vcc, s76, v82
	v_exp_f32_e32 v87, v83
	v_mov_b32_e32 v107, v99
	v_cndmask_b32_e32 v86, v134, v86, vcc
	v_cmp_ngt_f32_e32 vcc, -1.0, v82
	s_nop 1
	v_cndmask_b32_e32 v86, v135, v86, vcc
	v_cmp_neq_f32_e32 vcc, -1.0, v82
	s_nop 1
	v_cndmask_b32_e32 v86, v136, v86, vcc
	v_cmp_lt_f32_e64 vcc, |v82|, s77
	s_nop 1
	v_cndmask_b32_e32 v82, v86, v82, vcc
	v_add_f32_e32 v86, 1.0, v87
	v_mul_f32_e32 v143, 0xc1000000, v82
	v_add_f32_e32 v82, -1.0, v86
	v_sub_f32_e32 v83, v82, v86
	v_add_f32_e32 v83, 1.0, v83
	v_sub_f32_e32 v82, v87, v82
	v_add_f32_e32 v88, v82, v83
	v_frexp_mant_f32_e32 v89, v86
	v_cvt_f64_f32_e32 v[82:83], v86
	v_frexp_exp_i32_f64_e32 v82, v[82:83]
	v_cmp_gt_f32_e32 vcc, s74, v89
	s_nop 1
	v_subbrev_co_u32_e32 v82, vcc, 0, v82, vcc
	v_sub_u32_e32 v83, 0, v82
	v_ldexp_f32 v86, v86, v83
	v_ldexp_f32 v83, v88, v83
	v_add_f32_e32 v88, -1.0, v86
	v_add_f32_e32 v93, 1.0, v86
	v_add_f32_e32 v89, 1.0, v88
	v_add_f32_e32 v94, -1.0, v93
	v_sub_f32_e32 v89, v86, v89
	v_sub_f32_e32 v86, v86, v94
	v_add_f32_e32 v89, v83, v89
	v_add_f32_e32 v83, v83, v86
	v_add_f32_e32 v86, v93, v83
	v_rcp_f32_e32 v94, v86
	v_add_f32_e32 v92, v88, v89
	v_sub_f32_e32 v88, v92, v88
	v_sub_f32_e32 v88, v89, v88
	v_sub_f32_e32 v89, v86, v93
	v_sub_f32_e32 v83, v83, v89
	v_mul_f32_e32 v89, v92, v94
	v_mul_f32_e32 v93, v86, v89
	v_fma_f32 v95, v89, v86, -v93
	v_fmac_f32_e32 v95, v89, v83
	v_add_f32_e32 v96, v93, v95
	v_sub_f32_e32 v97, v92, v96
	v_sub_f32_e32 v92, v92, v97
	v_sub_f32_e32 v93, v96, v93
	v_sub_f32_e32 v92, v92, v96
	v_add_f32_e32 v88, v88, v92
	v_sub_f32_e32 v92, v93, v95
	v_add_f32_e32 v88, v92, v88
	v_add_f32_e32 v92, v97, v88
	v_mul_f32_e32 v93, v94, v92
	v_mul_f32_e32 v95, v86, v93
	v_fma_f32 v86, v93, v86, -v95
	v_fmac_f32_e32 v86, v93, v83
	v_sub_f32_e32 v83, v97, v92
	v_add_f32_e32 v83, v88, v83
	v_add_f32_e32 v88, v95, v86
	v_sub_f32_e32 v96, v92, v88
	v_sub_f32_e32 v92, v92, v96
	v_sub_f32_e32 v95, v88, v95
	v_sub_f32_e32 v88, v92, v88
	v_add_f32_e32 v83, v83, v88
	v_sub_f32_e32 v86, v95, v86
	v_cvt_f32_i32_e32 v82, v82
	v_add_f32_e32 v83, v86, v83
	v_add_f32_e32 v86, v89, v93
	v_add_f32_e32 v83, v96, v83
	v_sub_f32_e32 v88, v86, v89
	v_mul_f32_e32 v83, v94, v83
	v_sub_f32_e32 v88, v93, v88
	v_add_f32_e32 v83, v88, v83
	v_mul_f32_e32 v93, 0x3f317218, v82
	v_add_f32_e32 v88, v86, v83
	v_fma_f32 v94, v82, s75, -v93
	v_mul_f32_e32 v89, v88, v88
	v_fmac_f32_e32 v94, 0xb102e308, v82
	v_sub_f32_e32 v82, v88, v86
	v_fmamk_f32 v92, v89, 0x3e9b6dac, v133
	v_sub_f32_e32 v82, v83, v82
	v_add_f32_e32 v83, v93, v94
	v_fmaak_f32 v92, v89, v92, 0x3f2aaada
	v_sub_f32_e32 v86, v83, v93
	v_ldexp_f32 v93, v88, 1
	v_mul_f32_e32 v88, v88, v89
	v_mul_f32_e32 v88, v88, v92
	v_add_f32_e32 v89, v93, v88
	v_sub_f32_e32 v92, v89, v93
	v_ldexp_f32 v82, v82, 1
	v_sub_f32_e32 v88, v88, v92
	v_add_f32_e32 v82, v82, v88
	v_add_f32_e32 v88, v89, v82
	v_sub_f32_e32 v89, v88, v89
	v_sub_f32_e32 v82, v82, v89
	v_add_f32_e32 v89, v83, v88
	v_sub_f32_e32 v92, v89, v83
	v_sub_f32_e32 v93, v89, v92
	v_sub_f32_e32 v86, v94, v86
	v_sub_f32_e32 v83, v83, v93
	v_sub_f32_e32 v88, v88, v92
	v_add_f32_e32 v83, v88, v83
	v_add_f32_e32 v88, v86, v82
	v_sub_f32_e32 v92, v88, v86
	v_sub_f32_e32 v93, v88, v92
	v_sub_f32_e32 v86, v86, v93
	v_sub_f32_e32 v82, v82, v92
	v_add_f32_e32 v83, v88, v83
	v_add_f32_e32 v82, v82, v86
	v_add_f32_e32 v86, v89, v83
	v_sub_f32_e32 v88, v86, v89
	v_sub_f32_e32 v83, v83, v88
	v_add_f32_e32 v82, v82, v83
	v_mul_f32_e32 v83, 0xbfb8aa3b, v84
	v_add_f32_e32 v82, v86, v82
	v_cmp_neq_f32_e32 vcc, s76, v87
	v_exp_f32_e32 v84, v83
	s_nop 0
	v_cndmask_b32_e32 v82, v134, v82, vcc
	v_cmp_ngt_f32_e32 vcc, -1.0, v87
	v_add_f32_e32 v86, 1.0, v84
	v_frexp_mant_f32_e32 v88, v86
	v_cndmask_b32_e32 v82, v135, v82, vcc
	v_cmp_neq_f32_e32 vcc, -1.0, v87
	s_nop 1
	v_cndmask_b32_e32 v82, v136, v82, vcc
	v_cmp_lt_f32_e64 vcc, |v87|, s77
	s_nop 1
	v_cndmask_b32_e32 v82, v82, v87, vcc
	v_mul_f32_e32 v144, 0xc1000000, v82
	v_add_f32_e32 v82, -1.0, v86
	v_sub_f32_e32 v83, v82, v86
	v_add_f32_e32 v83, 1.0, v83
	v_sub_f32_e32 v82, v84, v82
	v_add_f32_e32 v87, v82, v83
	v_cvt_f64_f32_e32 v[82:83], v86
	v_frexp_exp_i32_f64_e32 v82, v[82:83]
	v_cmp_gt_f32_e32 vcc, s74, v88
	s_nop 1
	v_subbrev_co_u32_e32 v82, vcc, 0, v82, vcc
	v_sub_u32_e32 v83, 0, v82
	v_ldexp_f32 v86, v86, v83
	v_ldexp_f32 v83, v87, v83
	v_add_f32_e32 v87, -1.0, v86
	v_add_f32_e32 v92, 1.0, v86
	v_add_f32_e32 v88, 1.0, v87
	v_add_f32_e32 v93, -1.0, v92
	v_sub_f32_e32 v88, v86, v88
	v_sub_f32_e32 v86, v86, v93
	v_add_f32_e32 v88, v83, v88
	v_add_f32_e32 v83, v83, v86
	v_add_f32_e32 v86, v92, v83
	v_rcp_f32_e32 v93, v86
	v_add_f32_e32 v89, v87, v88
	v_sub_f32_e32 v87, v89, v87
	v_sub_f32_e32 v87, v88, v87
	v_sub_f32_e32 v88, v86, v92
	v_sub_f32_e32 v83, v83, v88
	v_mul_f32_e32 v88, v89, v93
	v_mul_f32_e32 v92, v86, v88
	v_fma_f32 v94, v88, v86, -v92
	v_fmac_f32_e32 v94, v88, v83
	v_add_f32_e32 v95, v92, v94
; __device__ __forceinline__ void unit(LAS unsigned char* lds, const bf16* __restrict__ xr, const bf16* __restrict__ yg, const float* __restrict__ conv_w, const float* __restrict__ conv_b, const bf16* __restrict__ wga_t, const bf16* __restrict__ wgx_t, ...
;     ...
;     for (int dt = 0; dt < 2; ++dt)
; #pragma unroll
;         for (int r = 0; r < 4; ++r) { const int c = n * 128 + hf * 64 + dq * 32 + 16 * dt + 4 * l4 + r; cba[dt][r] = b_ga[c]; cbx[dt][r] = b_gx[c]; csp[dt][r] = -8.0f * log1pf(__expf(-lam[c])); }
	v_sub_f32_e32 v96, v89, v95
	v_sub_f32_e32 v89, v89, v96
	v_sub_f32_e32 v92, v95, v92
	v_sub_f32_e32 v89, v89, v95
	v_add_f32_e32 v87, v87, v89
	v_sub_f32_e32 v89, v92, v94
	v_add_f32_e32 v87, v89, v87
	v_add_f32_e32 v89, v96, v87
	v_mul_f32_e32 v92, v93, v89
	v_mul_f32_e32 v94, v86, v92
	v_fma_f32 v86, v92, v86, -v94
	v_fmac_f32_e32 v86, v92, v83
	v_sub_f32_e32 v83, v96, v89
	v_add_f32_e32 v83, v87, v83
	v_add_f32_e32 v87, v94, v86
	v_sub_f32_e32 v95, v89, v87
	v_sub_f32_e32 v89, v89, v95
	v_sub_f32_e32 v94, v87, v94
	v_sub_f32_e32 v87, v89, v87
	v_add_f32_e32 v83, v83, v87
	v_sub_f32_e32 v86, v94, v86
	v_cvt_f32_i32_e32 v82, v82
	v_add_f32_e32 v83, v86, v83
	v_add_f32_e32 v86, v88, v92
	v_add_f32_e32 v83, v95, v83
	v_sub_f32_e32 v87, v86, v88
	v_mul_f32_e32 v83, v93, v83
	v_sub_f32_e32 v87, v92, v87
	v_add_f32_e32 v83, v87, v83
	v_mul_f32_e32 v92, 0x3f317218, v82
	v_add_f32_e32 v87, v86, v83
	v_fma_f32 v93, v82, s75, -v92
	v_mul_f32_e32 v88, v87, v87
	v_fmac_f32_e32 v93, 0xb102e308, v82
	v_sub_f32_e32 v82, v87, v86
	v_fmamk_f32 v89, v88, 0x3e9b6dac, v133
	v_sub_f32_e32 v82, v83, v82
	v_add_f32_e32 v83, v92, v93
	v_fmaak_f32 v89, v88, v89, 0x3f2aaada
	v_sub_f32_e32 v86, v83, v92
	v_ldexp_f32 v92, v87, 1
	v_mul_f32_e32 v87, v87, v88
	v_mul_f32_e32 v87, v87, v89
	v_add_f32_e32 v88, v92, v87
	v_sub_f32_e32 v89, v88, v92
	v_ldexp_f32 v82, v82, 1
	v_sub_f32_e32 v87, v87, v89
	v_add_f32_e32 v82, v82, v87
	v_add_f32_e32 v87, v88, v82
	v_sub_f32_e32 v88, v87, v88
	v_sub_f32_e32 v82, v82, v88
	v_add_f32_e32 v88, v83, v87
	v_sub_f32_e32 v89, v88, v83
	v_sub_f32_e32 v92, v88, v89
	v_sub_f32_e32 v86, v93, v86
	v_sub_f32_e32 v83, v83, v92
	v_sub_f32_e32 v87, v87, v89
	v_add_f32_e32 v83, v87, v83
	v_add_f32_e32 v87, v86, v82
	v_sub_f32_e32 v89, v87, v86
	v_sub_f32_e32 v92, v87, v89
	v_sub_f32_e32 v86, v86, v92
	v_sub_f32_e32 v82, v82, v89
	v_add_f32_e32 v83, v87, v83
	v_add_f32_e32 v82, v82, v86
	v_add_f32_e32 v86, v88, v83
	v_sub_f32_e32 v87, v86, v88
	v_sub_f32_e32 v83, v83, v87
	v_add_f32_e32 v82, v82, v83
	v_mul_f32_e32 v83, 0xbfb8aa3b, v85
	v_add_f32_e32 v82, v86, v82
	v_cmp_neq_f32_e32 vcc, s76, v84
	v_exp_f32_e32 v94, v83
	s_nop 0
	v_cndmask_b32_e32 v82, v134, v82, vcc
	v_cmp_ngt_f32_e32 vcc, -1.0, v84
	s_nop 1
	v_cndmask_b32_e32 v82, v135, v82, vcc
	v_cmp_neq_f32_e32 vcc, -1.0, v84
	s_nop 1
	v_cndmask_b32_e32 v82, v136, v82, vcc
	v_cmp_lt_f32_e64 vcc, |v84|, s77
	s_nop 1
	v_cndmask_b32_e32 v82, v82, v84, vcc
	v_add_f32_e32 v84, 1.0, v94
	v_mul_f32_e32 v145, 0xc1000000, v82
	v_add_f32_e32 v82, -1.0, v84
	v_sub_f32_e32 v83, v82, v84
	v_add_f32_e32 v83, 1.0, v83
	v_sub_f32_e32 v82, v94, v82
	v_add_f32_e32 v85, v82, v83
	v_frexp_mant_f32_e32 v86, v84
	v_cvt_f64_f32_e32 v[82:83], v84
	v_frexp_exp_i32_f64_e32 v82, v[82:83]
	v_cmp_gt_f32_e32 vcc, s74, v86
	s_nop 1
	v_subbrev_co_u32_e32 v82, vcc, 0, v82, vcc
	v_sub_u32_e32 v83, 0, v82
	v_ldexp_f32 v84, v84, v83
	v_ldexp_f32 v83, v85, v83
	v_add_f32_e32 v85, -1.0, v84
	v_add_f32_e32 v88, 1.0, v84
	v_add_f32_e32 v86, 1.0, v85
	v_add_f32_e32 v89, -1.0, v88
	v_sub_f32_e32 v86, v84, v86
	v_sub_f32_e32 v84, v84, v89
	v_add_f32_e32 v86, v83, v86
	v_add_f32_e32 v83, v83, v84
	v_add_f32_e32 v84, v88, v83
	v_rcp_f32_e32 v89, v84
	v_add_f32_e32 v87, v85, v86
	v_sub_f32_e32 v85, v87, v85
	v_sub_f32_e32 v85, v86, v85
	v_sub_f32_e32 v86, v84, v88
	v_sub_f32_e32 v83, v83, v86
	v_mul_f32_e32 v86, v87, v89
	v_mul_f32_e32 v88, v84, v86
	v_fma_f32 v92, v86, v84, -v88
	v_fmac_f32_e32 v92, v86, v83
	v_add_f32_e32 v93, v88, v92
	v_sub_f32_e32 v95, v87, v93
	v_sub_f32_e32 v87, v87, v95
	v_sub_f32_e32 v88, v93, v88
	v_sub_f32_e32 v87, v87, v93
	v_add_f32_e32 v85, v85, v87
	v_sub_f32_e32 v87, v88, v92
	v_add_f32_e32 v85, v87, v85
	v_add_f32_e32 v87, v95, v85
	v_mul_f32_e32 v88, v89, v87
	v_mul_f32_e32 v92, v84, v88
	v_fma_f32 v84, v88, v84, -v92
	v_fmac_f32_e32 v84, v88, v83
	v_sub_f32_e32 v83, v95, v87
	v_add_f32_e32 v83, v85, v83
	v_add_f32_e32 v85, v92, v84
	v_sub_f32_e32 v93, v87, v85
	v_sub_f32_e32 v87, v87, v93
	v_sub_f32_e32 v92, v85, v92
	v_sub_f32_e32 v85, v87, v85
	v_add_f32_e32 v83, v83, v85
	v_sub_f32_e32 v84, v92, v84
	v_cvt_f32_i32_e32 v82, v82
	v_add_f32_e32 v83, v84, v83
	v_add_f32_e32 v84, v86, v88
	v_add_f32_e32 v83, v93, v83
	v_sub_f32_e32 v85, v84, v86
	v_mul_f32_e32 v83, v89, v83
	v_sub_f32_e32 v85, v88, v85
	v_add_f32_e32 v83, v85, v83
	v_mul_f32_e32 v88, 0x3f317218, v82
	v_add_f32_e32 v85, v84, v83
	v_fma_f32 v89, v82, s75, -v88
	v_mul_f32_e32 v86, v85, v85
	v_fmac_f32_e32 v89, 0xb102e308, v82
	v_sub_f32_e32 v82, v85, v84
	v_fmamk_f32 v87, v86, 0x3e9b6dac, v133
	v_sub_f32_e32 v82, v83, v82
	v_add_f32_e32 v83, v88, v89
	v_fmaak_f32 v87, v86, v87, 0x3f2aaada
	v_sub_f32_e32 v84, v83, v88
	v_ldexp_f32 v88, v85, 1
	v_mul_f32_e32 v85, v85, v86
	v_mul_f32_e32 v85, v85, v87
	v_add_f32_e32 v86, v88, v85
	v_sub_f32_e32 v87, v86, v88
	v_ldexp_f32 v82, v82, 1
	v_sub_f32_e32 v85, v85, v87
	v_add_f32_e32 v82, v82, v85
	v_add_f32_e32 v85, v86, v82
	v_sub_f32_e32 v86, v85, v86
	v_sub_f32_e32 v82, v82, v86
	v_add_f32_e32 v86, v83, v85
	v_sub_f32_e32 v87, v86, v83
	v_sub_f32_e32 v88, v86, v87
	v_sub_f32_e32 v84, v89, v84
	v_sub_f32_e32 v83, v83, v88
	v_sub_f32_e32 v85, v85, v87
	v_add_f32_e32 v83, v85, v83
	v_add_f32_e32 v85, v84, v82
	v_sub_f32_e32 v87, v85, v84
	v_sub_f32_e32 v88, v85, v87
	v_sub_f32_e32 v84, v84, v88
	v_sub_f32_e32 v82, v82, v87
	v_add_f32_e32 v83, v85, v83
	v_add_f32_e32 v82, v82, v84
	v_add_f32_e32 v84, v86, v83
	v_sub_f32_e32 v85, v84, v86
	v_sub_f32_e32 v83, v83, v85
	v_add_f32_e32 v82, v82, v83
	v_add_f32_e32 v95, v84, v82
	v_add_co_u32_e32 v82, vcc, s29, v90
	v_lshl_add_u64 v[88:89], s[6:7], 0, v[106:107]
; #define LAS __attribute__((address_space(3)))
; __device__ __forceinline__ unsigned cvtpk(float lo, float hi) { const f32x2 v = {lo, hi}; return __builtin_bit_cast(unsigned, __builtin_convertvector(v, bf16x2_t)); }
; #define LRU_LOADX(t0) do { _Pragma("unroll") for (int k = 0; k < 11; ++k) { const int trow = (t0) + 8 * wave - 3 + k; xq[k] = trow >= 0 ? xrp[((ptrdiff_t)((t0) - 3 + k)) * 512] : 0u; } \
;         _Pragma("unroll") for (int i = 0; i < 8; ++i) yv[i] = ygp[((size_t)(t0) + i) * 1024]; } while (0)
; __device__ __forceinline__ void unit(LAS unsigned char* lds, const bf16* __restrict__ xr, const bf16* __restrict__ yg, const float* __restrict__ conv_w, const float* __restrict__ conv_b, const bf16* __restrict__ wga_t, const bf16* __restrict__ wgx_t, ...
;     ...
;     LRU_LOADX(0);
;     asm volatile("s_waitcnt lgkmcnt(0)" ::: "memory"); __builtin_amdgcn_s_barrier(); asm volatile("" ::: "memory");
; #pragma unroll 1
;     for (int t0 = 0; t0 < SEQ; t0 += 64) {
;         { f32x2 xe[11];
; #pragma unroll
;           for (int k = 0; k < 11; ++k) xe[k] = (f32x2){__uint_as_float(xq[k] << 16), __uint_as_float(xq[k] & 0xffff0000u)};
; #pragma unroll
;           for (int i = 0; i < 8; ++i) { f32x2 xc2 = (f32x2){cb0, cb1};
; #pragma unroll
;             for (int jj = 0; jj < 4; ++jj) xc2 += (f32x2){cw0[jj], cw1[jj]} * xe[i + jj];
;             *(LAS unsigned*)(lds + XA_OFF + (8 * wave + i) * XA_P + 4 * lane) = cvtpk(xc2.x, xc2.y);
;             if ((lane >> 5) == hf) *(LAS f32x2*)(XF + (8 * wave + i) * 64 + 2 * (lane & 31)) = xc2; } }
	s_nop 0
	v_addc_co_u32_e32 v83, vcc, 0, v91, vcc
	v_add_co_u32_e32 v84, vcc, s72, v90
	s_nop 1
	v_addc_co_u32_e32 v85, vcc, 0, v91, vcc
	v_add_co_u32_e32 v86, vcc, s73, v90
	s_nop 1
	v_addc_co_u32_e32 v87, vcc, 0, v91, vcc
	v_add_co_u32_e32 v92, vcc, s72, v88
	s_nop 1
	v_addc_co_u32_e32 v93, vcc, 0, v89, vcc
	global_load_dword v146, v[84:85], off offset:-4096
	global_load_dword v157, v[84:85], off
	global_load_dword v158, v[84:85], off offset:2048
	global_load_ushort v177, v106, s[6:7]
	global_load_ushort v171, v[92:93], off offset:-4096
	global_load_ushort v165, v[92:93], off
	global_load_ushort v164, v[92:93], off offset:2048
	global_load_ushort v176, v106, s[6:7] offset:2048
	v_add_co_u32_e32 v84, vcc, s29, v88
	v_cmp_eq_u32_e64 s[6:7], s42, v127
	s_nop 0
	v_addc_co_u32_e32 v85, vcc, 0, v89, vcc
	v_add_co_u32_e32 v88, vcc, s73, v88
	s_lshl_b32 s42, s34, 4
	s_nop 0
	v_addc_co_u32_e32 v89, vcc, 0, v89, vcc
	global_load_dword v147, v[90:91], off
	global_load_dword v150, v[90:91], off offset:2048
	global_load_dword v151, v[82:83], off offset:2048
	global_load_dword v159, v[86:87], off
	global_load_dword v160, v[86:87], off offset:2048
	global_load_ushort v166, v[84:85], off offset:2048
	global_load_ushort v163, v[88:89], off
	global_load_ushort v162, v[88:89], off offset:2048
	v_and_or_b32 v83, s42, 48, v148
	s_and_b32 s42, s66, 0x1fffffc0
	s_cmp_eq_u32 s34, 7
	v_lshl_add_u32 v149, s42, 3, v129
	s_cselect_b64 s[42:43], -1, 0
	s_or_b32 s54, s51, 1
	s_lshl_b32 s51, s51, 8
	s_lshl_b32 s80, s34, 11
	s_lshl_b32 s82, s54, 8
	s_or_b32 s83, s51, 0x200
	s_or_b32 s84, s51, 0x300
	s_or_b32 s85, s51, 0x400
	s_or_b32 s86, s51, 0x500
	s_or_b32 s87, s51, 0x600
	s_or_b32 s88, s51, 0x700
	s_cmpk_gt_u32 s66, 0x7f
	s_cselect_b64 s[50:51], -1, 0
	s_cmpk_gt_u32 s66, 0xbf
	s_mul_i32 s81, s54, 0x110
	s_cselect_b64 s[54:55], -1, 0
	s_cmpk_gt_u32 s66, 0xff
	s_cselect_b64 s[60:61], -1, 0
	s_cmpk_gt_u32 s66, 0x13f
	s_cselect_b64 s[62:63], -1, 0
	s_cmpk_gt_u32 s66, 0x17f
	v_cmp_neq_f32_e32 vcc, s76, v94
	v_or_b32_e32 v85, s52, v103
	s_cselect_b64 s[64:65], -1, 0
	s_cmpk_gt_u32 s66, 0x1bf
	v_cndmask_b32_e32 v82, v134, v95, vcc
	v_cmp_ngt_f32_e32 vcc, -1.0, v94
	v_lshlrev_b32_e32 v86, 8, v83
	v_lshlrev_b32_e32 v85, 2, v85
	s_cselect_b64 s[66:67], -1, 0
	s_lshl_b64 s[70:71], s[68:69], 22
	s_lshl_b64 s[90:91], s[34:35], 14
	v_cndmask_b32_e32 v82, v135, v82, vcc
	v_cmp_neq_f32_e32 vcc, -1.0, v94
	v_add3_u32 v152, 0, v86, v85
	s_add_u32 s70, s90, s70
	v_cndmask_b32_e32 v82, v136, v82, vcc
	v_cmp_lt_f32_e64 vcc, |v94|, s77
	v_mul_u32_u24_e32 v84, 0x110, v83
	v_lshl_add_u32 v153, v83, 4, v152
	s_addc_u32 s71, s91, s71
	v_or_b32_e32 v83, s70, v102
	v_cndmask_b32_e32 v82, v82, v94, vcc
	v_mov_b32_e32 v119, s71
	v_or_b32_e32 v118, s89, v83
	v_mov_b32_e32 v121, s71
	v_or_b32_e32 v83, s70, v100
	s_lshl_b64 s[70:71], s[68:69], 23
	s_lshl_b64 s[90:91], s[34:35], 15
	v_mul_f32_e32 v107, 0xc1000000, v82
	v_cndmask_b32_e64 v82, 0, 1, s[56:57]
	s_add_u32 s70, s90, s70
	v_lshlrev_b32_e32 v82, 7, v82
	v_or_b32_e32 v83, s89, v83
	s_addc_u32 s71, s91, s71
	v_or_b32_e32 v120, v83, v82
	v_mov_b32_e32 v123, s71
	v_or_b32_e32 v83, s70, v100
	s_lshl_b64 s[68:69], s[68:69], 17
	s_lshl_b64 s[70:71], s[34:35], 9
	s_add_u32 s34, s68, s70
	s_waitcnt lgkmcnt(0)
	s_barrier
	s_addc_u32 s68, s69, s71
	s_or_b32 s34, s34, s92
	v_or_b32_e32 v83, s89, v83
	s_add_u32 s34, s34, 0x2a00100
	v_or_b32_e32 v122, v83, v82
	s_addc_u32 s89, s68, 0
	s_movk_i32 s90, 0xffc0
	v_add_u32_e32 v161, v130, v84
	s_waitcnt vmcnt(0)
	s_branch .LBB5_937
.LBB5_936:
	s_mov_b64 s[70:71], 0x40000
	s_add_u32 s34, s34, 0x1000
	v_lshl_add_u64 v[118:119], v[118:119], 0, s[96:97]
	v_lshl_add_u64 v[120:121], v[120:121], 0, s[96:97]
	v_lshl_add_u64 v[122:123], v[122:123], 0, s[70:71]
	s_addc_u32 s89, s89, 0
	s_andn2_b64 vcc, exec, s[68:69]
	s_waitcnt vmcnt(16)
	v_mov_b32_e32 v177, v167
	v_mov_b32_e32 v176, v168
	v_mov_b32_e32 v171, v169
	v_mov_b32_e32 v166, v170
	v_mov_b32_e32 v165, v172
	v_mov_b32_e32 v164, v173
	v_mov_b32_e32 v163, v174
	v_mov_b32_e32 v162, v175
	s_cbranch_vccz .LBB5_928
.LBB5_937:
	v_lshlrev_b32_e32 v84, 16, v137
	v_and_b32_e32 v85, 0xffff0000, v137
	v_lshlrev_b32_e32 v88, 16, v98
	v_and_b32_e32 v89, 0xffff0000, v98
	v_pk_fma_f32 v[84:85], v[112:113], v[84:85], v[114:115]
	v_lshlrev_b32_e32 v86, 16, v138
	v_and_b32_e32 v87, 0xffff0000, v138
	v_pk_fma_f32 v[84:85], v[108:109], v[88:89], v[84:85]
	v_lshlrev_b32_e32 v82, 16, v147
	v_and_b32_e32 v83, 0xffff0000, v147
	v_pk_fma_f32 v[84:85], v[110:111], v[86:87], v[84:85]
	s_nop 0
	v_pk_fma_f32 v[84:85], v[116:117], v[82:83], v[84:85]
	s_nop 0
	v_cvt_pk_bf16_f32 v90, v84, v85
	ds_write_b32 v156, v90
	s_and_saveexec_b64 s[68:69], s[6:7]
	v_add_u32_e32 v90, s80, v128
	ds_write_b64 v90, v[84:85] offset:17408
	s_or_b64 exec, exec, s[68:69]
	v_pk_fma_f32 v[88:89], v[112:113], v[88:89], v[114:115]
	v_lshlrev_b32_e32 v84, 16, v150
	v_pk_fma_f32 v[88:89], v[108:109], v[86:87], v[88:89]
	v_and_b32_e32 v85, 0xffff0000, v150
	v_pk_fma_f32 v[88:89], v[110:111], v[82:83], v[88:89]
	v_add_u32_e32 v90, s81, v126
	v_pk_fma_f32 v[88:89], v[116:117], v[84:85], v[88:89]
	s_nop 0
	v_cvt_pk_bf16_f32 v91, v88, v89
	ds_write_b32 v90, v91
	s_and_saveexec_b64 s[68:69], s[6:7]
	v_add_u32_e32 v91, s82, v128
	ds_write_b64 v91, v[88:89] offset:17408
	s_or_b64 exec, exec, s[68:69]
	v_pk_fma_f32 v[86:87], v[112:113], v[86:87], v[114:115]
	v_lshlrev_b32_e32 v88, 16, v146
	v_pk_fma_f32 v[86:87], v[108:109], v[82:83], v[86:87]
	v_and_b32_e32 v89, 0xffff0000, v146
	v_pk_fma_f32 v[86:87], v[110:111], v[84:85], v[86:87]
	s_nop 0
	v_pk_fma_f32 v[86:87], v[116:117], v[88:89], v[86:87]
	s_nop 0
; #define LAS __attribute__((address_space(3)))
; __device__ __forceinline__ unsigned cvtpk(float lo, float hi) { const f32x2 v = {lo, hi}; return __builtin_bit_cast(unsigned, __builtin_convertvector(v, bf16x2_t)); }
; #define LRU_LOADX(t0) do { _Pragma("unroll") for (int k = 0; k < 11; ++k) { const int trow = (t0) + 8 * wave - 3 + k; xq[k] = trow >= 0 ? xrp[((ptrdiff_t)((t0) - 3 + k)) * 512] : 0u; } \
;         _Pragma("unroll") for (int i = 0; i < 8; ++i) yv[i] = ygp[((size_t)(t0) + i) * 1024]; } while (0)
; __device__ __forceinline__ void unit(LAS unsigned char* lds, const bf16* __restrict__ xr, const bf16* __restrict__ yg, const float* __restrict__ conv_w, const float* __restrict__ conv_b, const bf16* __restrict__ wga_t, const bf16* __restrict__ wgx_t, ...
;     ...
;         { f32x2 xe[11];
; #pragma unroll
;           for (int k = 0; k < 11; ++k) xe[k] = (f32x2){__uint_as_float(xq[k] << 16), __uint_as_float(xq[k] & 0xffff0000u)};
; #pragma unroll
;           for (int i = 0; i < 8; ++i) { f32x2 xc2 = (f32x2){cb0, cb1};
; #pragma unroll
;             for (int jj = 0; jj < 4; ++jj) xc2 += (f32x2){cw0[jj], cw1[jj]} * xe[i + jj];
;             *(LAS unsigned*)(lds + XA_OFF + (8 * wave + i) * XA_P + 4 * lane) = cvtpk(xc2.x, xc2.y);
;             if ((lane >> 5) == hf) *(LAS f32x2*)(XF + (8 * wave + i) * 64 + 2 * (lane & 31)) = xc2; } }
;         bf16 ycur[8];
; #pragma unroll
;         for (int i = 0; i < 8; ++i) ycur[i] = yv[i];
;         if (t0 + 64 < SEQ) LRU_LOADX(t0 + 64);
	v_cvt_pk_bf16_f32 v91, v86, v87
	ds_write_b32 v90, v91 offset:272
	s_and_saveexec_b64 s[68:69], s[6:7]
	v_add_u32_e32 v91, s83, v128
	ds_write_b64 v91, v[86:87] offset:17408
	s_or_b64 exec, exec, s[68:69]
	v_pk_fma_f32 v[82:83], v[112:113], v[82:83], v[114:115]
	v_lshlrev_b32_e32 v86, 16, v151
	v_pk_fma_f32 v[82:83], v[108:109], v[84:85], v[82:83]
	v_and_b32_e32 v87, 0xffff0000, v151
	v_pk_fma_f32 v[82:83], v[110:111], v[88:89], v[82:83]
	s_nop 0
	v_pk_fma_f32 v[82:83], v[116:117], v[86:87], v[82:83]
	s_nop 0
	v_cvt_pk_bf16_f32 v91, v82, v83
	ds_write_b32 v90, v91 offset:544
	s_and_saveexec_b64 s[68:69], s[6:7]
	v_add_u32_e32 v91, s84, v128
	ds_write_b64 v91, v[82:83] offset:17408
	s_or_b64 exec, exec, s[68:69]
	v_pk_fma_f32 v[84:85], v[112:113], v[84:85], v[114:115]
	v_lshlrev_b32_e32 v82, 16, v157
	v_pk_fma_f32 v[84:85], v[108:109], v[88:89], v[84:85]
	v_and_b32_e32 v83, 0xffff0000, v157
	v_pk_fma_f32 v[84:85], v[110:111], v[86:87], v[84:85]
	s_nop 0
	v_pk_fma_f32 v[84:85], v[116:117], v[82:83], v[84:85]
	s_nop 0
	v_cvt_pk_bf16_f32 v91, v84, v85
	ds_write_b32 v90, v91 offset:816
	s_and_saveexec_b64 s[68:69], s[6:7]
	v_add_u32_e32 v91, s85, v128
	ds_write_b64 v91, v[84:85] offset:17408
	s_or_b64 exec, exec, s[68:69]
	v_pk_fma_f32 v[88:89], v[112:113], v[88:89], v[114:115]
	v_lshlrev_b32_e32 v84, 16, v158
	v_pk_fma_f32 v[88:89], v[108:109], v[86:87], v[88:89]
	v_and_b32_e32 v85, 0xffff0000, v158
	v_pk_fma_f32 v[88:89], v[110:111], v[82:83], v[88:89]
	s_nop 0
	v_pk_fma_f32 v[88:89], v[116:117], v[84:85], v[88:89]
	s_nop 0
	v_cvt_pk_bf16_f32 v91, v88, v89
	ds_write_b32 v90, v91 offset:1088
	s_and_saveexec_b64 s[68:69], s[6:7]
	v_add_u32_e32 v91, s86, v128
	ds_write_b64 v91, v[88:89] offset:17408
	s_or_b64 exec, exec, s[68:69]
	v_pk_fma_f32 v[86:87], v[112:113], v[86:87], v[114:115]
	v_lshlrev_b32_e32 v88, 16, v159
	v_pk_fma_f32 v[86:87], v[108:109], v[82:83], v[86:87]
	v_and_b32_e32 v89, 0xffff0000, v159
	v_pk_fma_f32 v[86:87], v[110:111], v[84:85], v[86:87]
	s_nop 0
	v_pk_fma_f32 v[86:87], v[116:117], v[88:89], v[86:87]
	s_nop 0
	v_cvt_pk_bf16_f32 v91, v86, v87
	ds_write_b32 v90, v91 offset:1360
	s_and_saveexec_b64 s[68:69], s[6:7]
	v_add_u32_e32 v91, s87, v128
	ds_write_b64 v91, v[86:87] offset:17408
	s_or_b64 exec, exec, s[68:69]
	v_pk_fma_f32 v[82:83], v[112:113], v[82:83], v[114:115]
	v_lshlrev_b32_e32 v86, 16, v160
	v_pk_fma_f32 v[82:83], v[108:109], v[84:85], v[82:83]
	v_and_b32_e32 v87, 0xffff0000, v160
	v_pk_fma_f32 v[82:83], v[110:111], v[88:89], v[82:83]
	s_nop 0
	v_pk_fma_f32 v[82:83], v[116:117], v[86:87], v[82:83]
	s_nop 0
	v_cvt_pk_bf16_f32 v84, v82, v83
	ds_write_b32 v90, v84 offset:1632
	s_and_saveexec_b64 s[68:69], s[6:7]
	v_add_u32_e32 v84, s88, v128
	ds_write_b64 v84, v[82:83] offset:17408
	s_or_b64 exec, exec, s[68:69]
	s_add_i32 s90, s90, 64
	s_cmpk_gt_u32 s90, 0x7bf
	s_cselect_b64 s[68:69], -1, 0
	s_and_b64 vcc, exec, s[68:69]
	v_mov_b32_e32 v167, v177
	v_mov_b32_e32 v168, v176
	v_mov_b32_e32 v169, v171
	v_mov_b32_e32 v170, v166
	v_mov_b32_e32 v172, v165
	v_mov_b32_e32 v173, v164
	v_mov_b32_e32 v174, v163
	v_mov_b32_e32 v175, v162
	s_cbranch_vccnz .LBB5_955
	v_lshl_add_u64 v[82:83], s[22:23], 0, v[118:119]
	v_add_co_u32_e32 v84, vcc, 0x4801e000, v82
	s_nop 1
	v_addc_co_u32_e32 v85, vcc, 0, v83, vcc
	global_load_dword v137, v[84:85], off offset:2048
	v_add_co_u32_e32 v84, vcc, 0x4801f000, v82
	s_nop 1
	v_addc_co_u32_e32 v85, vcc, 0, v83, vcc
	global_load_dword v98, v[84:85], off
	global_load_dword v138, v[84:85], off offset:2048
	v_add_co_u32_e32 v84, vcc, 0x48020000, v82
	s_nop 1
	v_addc_co_u32_e32 v85, vcc, 0, v83, vcc
	global_load_dword v147, v[84:85], off
	global_load_dword v150, v[84:85], off offset:2048
	v_add_co_u32_e32 v84, vcc, 0x48021000, v82
	s_nop 1
	v_addc_co_u32_e32 v85, vcc, 0, v83, vcc
	global_load_dword v146, v[84:85], off
	global_load_dword v151, v[84:85], off offset:2048
	v_add_co_u32_e32 v84, vcc, 0x48022000, v82
	s_nop 1
	v_addc_co_u32_e32 v85, vcc, 0, v83, vcc
	v_add_co_u32_e32 v82, vcc, 0x48023000, v82
	global_load_dword v157, v[84:85], off
	global_load_dword v158, v[84:85], off offset:2048
	v_addc_co_u32_e32 v83, vcc, 0, v83, vcc
	global_load_dword v159, v[82:83], off
	global_load_dword v160, v[82:83], off offset:2048
	v_lshl_add_u64 v[82:83], s[22:23], 0, v[120:121]
	v_add_co_u32_e32 v84, vcc, 0x4c020000, v82
	s_nop 1
	v_addc_co_u32_e32 v85, vcc, 0, v83, vcc
	global_load_ushort v167, v[84:85], off
	global_load_ushort v168, v[84:85], off offset:2048
	v_add_co_u32_e32 v84, vcc, 0x4c021000, v82
	s_nop 1
	v_addc_co_u32_e32 v85, vcc, 0, v83, vcc
	global_load_ushort v169, v[84:85], off
	global_load_ushort v170, v[84:85], off offset:2048
	v_add_co_u32_e32 v84, vcc, 0x4c022000, v82
	s_nop 1
	v_addc_co_u32_e32 v85, vcc, 0, v83, vcc
	v_add_co_u32_e32 v82, vcc, 0x4c023000, v82
	global_load_ushort v172, v[84:85], off
	global_load_ushort v173, v[84:85], off offset:2048
	v_addc_co_u32_e32 v83, vcc, 0, v83, vcc
	global_load_ushort v174, v[82:83], off
	global_load_ushort v175, v[82:83], off offset:2048
; #define LAS __attribute__((address_space(3)))
; #define MFMA16(a, b, c) __builtin_amdgcn_mfma_f32_16x16x32_bf16((a), (b), (c), 0, 0, 0)
; __device__ __forceinline__ float fsig(float x) { return __builtin_amdgcn_rcpf(1.0f + __builtin_amdgcn_exp2f(-LOG2E * x)); }
; __device__ __forceinline__ void unit(LAS unsigned char* lds, const bf16* __restrict__ xr, const bf16* __restrict__ yg, const float* __restrict__ conv_w, const float* __restrict__ conv_b, const bf16* __restrict__ wga_t, const bf16* __restrict__ wgx_t, ...
;     ...
;         {
;             f32x4 ar[2] = {}, ai[2] = {};
; #pragma unroll
;             for (int ks = 0; ks < 4; ++ks) { const bf16x8 xfr = *(const LAS bf16x8*)(lds + XA_OFF + (16 * tb + l15) * XA_P + 64 * ks + 16 * l4);
; #pragma unroll
;                 for (int dt = 0; dt < 2; ++dt) { ar[dt] = MFMA16(wf[0][dt][ks], xfr, ar[dt]); ai[dt] = MFMA16(wf[1][dt][ks], xfr, ai[dt]); } }
;             const int tk = 16 * tb + l15;
; #pragma unroll
;             for (int dt = 0; dt < 2; ++dt) { const int dl = dq * 32 + 16 * dt + 4 * l4; const f32x4 xo = *(const LAS f32x4*)(XF + tk * 64 + dl); f32x4 av, bv;
; #pragma unroll
;                 for (int r = 0; r < 4; ++r) { const float rg = fsig(ar[dt][r] + cba[dt][r]), ig = fsig(ai[dt][r] + cbx[dt][r]); const float la = rg * csp[dt][r];
;                     const float a_ = __builtin_amdgcn_exp2f(LOG2E * la); av[r] = a_;
;                     bv[r] = __builtin_amdgcn_sqrtf(fmaxf(1.0f - a_ * a_, 0.f)) * (ig * xo[r]); }
;                 *(LAS f32x4*)(SA + tk * 68 + dl) = av; *(LAS f32x4*)(SB + tk * 68 + dl) = bv; }
.LBB5_955:
	s_waitcnt lgkmcnt(0)
	s_barrier
	ds_read_b128 v[82:85], v161
	ds_read_b128 v[178:181], v161 offset:64
	ds_read_b128 v[214:217], v161 offset:128
	ds_read_b128 v[218:221], v161 offset:192
	s_and_b64 vcc, exec, s[4:5]
	s_waitcnt lgkmcnt(3)
	v_mfma_f32_16x16x32_bf16 v[86:89], v[2:5], v[82:85], 0
	v_mfma_f32_16x16x32_bf16 v[90:93], v[6:9], v[82:85], 0
	v_mfma_f32_16x16x32_bf16 v[94:97], v[34:37], v[82:85], 0
	v_mfma_f32_16x16x32_bf16 v[82:85], v[38:41], v[82:85], 0
	s_waitcnt lgkmcnt(2)
	v_mfma_f32_16x16x32_bf16 v[86:89], v[10:13], v[178:181], v[86:89]
	v_mfma_f32_16x16x32_bf16 v[90:93], v[14:17], v[178:181], v[90:93]
	v_mfma_f32_16x16x32_bf16 v[94:97], v[42:45], v[178:181], v[94:97]
	v_mfma_f32_16x16x32_bf16 v[82:85], v[46:49], v[178:181], v[82:85]
	s_waitcnt lgkmcnt(1)
	v_mfma_f32_16x16x32_bf16 v[86:89], v[18:21], v[214:217], v[86:89]
	v_mfma_f32_16x16x32_bf16 v[90:93], v[22:25], v[214:217], v[90:93]
	v_mfma_f32_16x16x32_bf16 v[182:185], v[50:53], v[214:217], v[94:97]
	v_mfma_f32_16x16x32_bf16 v[82:85], v[54:57], v[214:217], v[82:85]
	s_waitcnt lgkmcnt(0)
	v_mfma_f32_16x16x32_bf16 v[186:189], v[26:29], v[218:221], v[86:89]
	v_mfma_f32_16x16x32_bf16 v[94:97], v[30:33], v[218:221], v[90:93]
	s_nop 6
	v_add_f32_e32 v124, v66, v186
	v_mul_f32_e32 v124, 0xbfb8aa3b, v124
	v_exp_f32_e32 v124, v124
	v_mfma_f32_16x16x32_bf16 v[86:89], v[58:61], v[218:221], v[182:185]
	ds_read_b128 v[90:93], v152 offset:17408
	v_add_f32_e32 v94, v70, v94
	v_add_f32_e32 v96, v72, v96
	v_mfma_f32_16x16x32_bf16 v[82:85], v[62:65], v[218:221], v[82:85]
	v_add_f32_e32 v180, v68, v188
	v_mul_f32_e32 v180, 0xbfb8aa3b, v180
	v_exp_f32_e32 v180, v180
	v_mul_f32_e32 v94, 0xbfb8aa3b, v94
	v_mul_f32_e32 v96, 0xbfb8aa3b, v96
	v_add_f32_e32 v124, 1.0, v124
	v_exp_f32_e32 v94, v94
	v_add_f32_e32 v180, 1.0, v180
	v_exp_f32_e32 v96, v96
	v_rcp_f32_e32 v125, v124
	v_rcp_f32_e32 v181, v180
	v_add_f32_e32 v94, 1.0, v94
	v_add_f32_e32 v96, 1.0, v96
	v_rcp_f32_e32 v124, v94
	v_mul_f32_e32 v94, v139, v125
	v_rcp_f32_e32 v180, v96
	v_mul_f32_e32 v96, v141, v181
	v_mul_f32_e32 v94, 0x3fb8aa3b, v94
	v_mul_f32_e32 v96, 0x3fb8aa3b, v96
	v_exp_f32_e32 v94, v94
	v_exp_f32_e32 v96, v96
	v_add_f32_e32 v95, v71, v95
	v_add_f32_e32 v97, v73, v97
	v_fma_f32 v125, -v94, v94, 1.0
	v_fma_f32 v181, -v96, v96, 1.0
	v_max_f32_e32 v125, 0, v125
	v_max_f32_e32 v181, 0, v181
	v_sqrt_f32_e32 v178, v125
	v_add_f32_e32 v125, v67, v187
	v_sqrt_f32_e32 v182, v181
	v_add_f32_e32 v181, v69, v189
	v_mul_f32_e32 v125, 0xbfb8aa3b, v125
	v_mul_f32_e32 v181, 0xbfb8aa3b, v181
	v_exp_f32_e32 v125, v125
	v_exp_f32_e32 v181, v181
	v_mul_f32_e32 v95, 0xbfb8aa3b, v95
	v_mul_f32_e32 v97, 0xbfb8aa3b, v97
	v_add_f32_e32 v125, 1.0, v125
	v_exp_f32_e32 v95, v95
	v_add_f32_e32 v181, 1.0, v181
	v_exp_f32_e32 v97, v97
	v_rcp_f32_e32 v179, v125
	v_rcp_f32_e32 v183, v181
	v_add_f32_e32 v95, 1.0, v95
	v_add_f32_e32 v97, 1.0, v97
	v_rcp_f32_e32 v125, v95
	v_mul_f32_e32 v95, v140, v179
	v_rcp_f32_e32 v181, v97
	v_mul_f32_e32 v97, v142, v183
	v_mul_f32_e32 v95, 0x3fb8aa3b, v95
	v_mul_f32_e32 v97, 0x3fb8aa3b, v97
	v_exp_f32_e32 v95, v95
	v_exp_f32_e32 v97, v97
	v_add_f32_e32 v86, v74, v86
	v_add_f32_e32 v87, v75, v87
	v_add_f32_e32 v88, v76, v88
	v_add_f32_e32 v89, v77, v89
	v_fma_f32 v179, -v95, v95, 1.0
	v_fma_f32 v183, -v97, v97, 1.0
	v_mul_f32_e32 v86, 0xbfb8aa3b, v86
	v_mul_f32_e32 v87, 0xbfb8aa3b, v87
	v_mul_f32_e32 v88, 0xbfb8aa3b, v88
	v_mul_f32_e32 v89, 0xbfb8aa3b, v89
	v_max_f32_e32 v179, 0, v179
	v_max_f32_e32 v183, 0, v183
	v_exp_f32_e32 v86, v86
	v_exp_f32_e32 v87, v87
	v_exp_f32_e32 v88, v88
	v_exp_f32_e32 v89, v89
	v_sqrt_f32_e32 v179, v179
	v_sqrt_f32_e32 v183, v183
	v_add_f32_e32 v82, v78, v82
	v_add_f32_e32 v83, v79, v83
	v_add_f32_e32 v84, v80, v84
	v_add_f32_e32 v85, v81, v85
	v_mul_f32_e32 v82, 0xbfb8aa3b, v82
	v_mul_f32_e32 v83, 0xbfb8aa3b, v83
	v_mul_f32_e32 v84, 0xbfb8aa3b, v84
	v_mul_f32_e32 v85, 0xbfb8aa3b, v85
	s_waitcnt lgkmcnt(0)
	v_pk_mul_f32 v[90:91], v[90:91], v[124:125]
	v_pk_mul_f32 v[92:93], v[92:93], v[180:181]
	v_add_f32_e32 v86, 1.0, v86
	v_exp_f32_e32 v82, v82
	v_add_f32_e32 v87, 1.0, v87
	v_exp_f32_e32 v83, v83
	v_add_f32_e32 v88, 1.0, v88
	v_exp_f32_e32 v84, v84
	v_add_f32_e32 v89, 1.0, v89
	v_exp_f32_e32 v85, v85
	v_pk_mul_f32 v[92:93], v[92:93], v[182:183]
	v_pk_mul_f32 v[90:91], v[90:91], v[178:179]
	ds_write_b128 v153, v[94:97] offset:33792
	ds_write_b128 v153, v[90:93] offset:51200
	v_rcp_f32_e32 v94, v86
	v_rcp_f32_e32 v95, v87
	v_rcp_f32_e32 v96, v88
	v_rcp_f32_e32 v97, v89
	v_add_f32_e32 v82, 1.0, v82
	v_add_f32_e32 v83, 1.0, v83
	v_add_f32_e32 v84, 1.0, v84
	v_add_f32_e32 v85, 1.0, v85
	v_rcp_f32_e32 v86, v82
	v_mul_f32_e32 v82, v143, v94
	v_rcp_f32_e32 v87, v83
	v_mul_f32_e32 v83, v144, v95
	v_rcp_f32_e32 v88, v84
	v_mul_f32_e32 v84, v145, v96
	v_rcp_f32_e32 v89, v85
	v_mul_f32_e32 v85, v107, v97
	v_mul_f32_e32 v82, 0x3fb8aa3b, v82
	v_mul_f32_e32 v83, 0x3fb8aa3b, v83
	v_mul_f32_e32 v84, 0x3fb8aa3b, v84
	v_mul_f32_e32 v85, 0x3fb8aa3b, v85
	v_exp_f32_e32 v82, v82
	v_exp_f32_e32 v83, v83
	v_exp_f32_e32 v84, v84
	v_exp_f32_e32 v85, v85
	ds_read_b128 v[90:93], v152 offset:17472
	v_fma_f32 v94, -v82, v82, 1.0
	v_fma_f32 v95, -v83, v83, 1.0
	v_fma_f32 v96, -v84, v84, 1.0
	v_fma_f32 v97, -v85, v85, 1.0
	v_max_f32_e32 v94, 0, v94
	v_max_f32_e32 v95, 0, v95
	v_max_f32_e32 v96, 0, v96
	v_max_f32_e32 v97, 0, v97
	v_sqrt_f32_e32 v94, v94
	v_sqrt_f32_e32 v95, v95
	v_sqrt_f32_e32 v96, v96
	v_sqrt_f32_e32 v97, v97
	s_waitcnt lgkmcnt(0)
	v_pk_mul_f32 v[86:87], v[90:91], v[86:87]
	v_pk_mul_f32 v[88:89], v[92:93], v[88:89]
	v_pk_mul_f32 v[86:87], v[86:87], v[94:95]
	v_pk_mul_f32 v[88:89], v[88:89], v[96:97]
	ds_write_b128 v153, v[82:85] offset:33856
	ds_write_b128 v153, v[86:89] offset:51264
	s_waitcnt lgkmcnt(0)
	s_barrier
; __device__ __forceinline__ float bf2f(bf16 b) { return __uint_as_float(((unsigned)b) << 16); }
; __device__ __forceinline__ unsigned cvtpk(float lo, float hi) { const f32x2 v = {lo, hi}; return __builtin_bit_cast(unsigned, __builtin_convertvector(v, bf16x2_t)); }
; __device__ __forceinline__ void unit(LAS unsigned char* lds, const bf16* __restrict__ xr, const bf16* __restrict__ yg, const float* __restrict__ conv_w, const float* __restrict__ conv_b, const bf16* __restrict__ wga_t, const bf16* __restrict__ wgx_t, ...
;     ...
;         { float A = 1.f, B = 0.f;
; #pragma unroll
;             for (int i = 0; i < 8; ++i) { a8[i] = SA[(8 * sg + i) * 68 + cc]; b8[i] = SB[(8 * sg + i) * 68 + cc]; B = a8[i] * B + b8[i]; A *= a8[i]; }
;             SC[sg * 64 + cc] = (f32x2){A, B}; }
;         asm volatile("s_waitcnt lgkmcnt(0)" ::: "memory"); __builtin_amdgcn_s_barrier(); asm volatile("" ::: "memory");
;         {
;             float hcur = HS[cc];
; #pragma unroll
;             for (int s2 = 0; s2 < 7; ++s2) { const f32x2 ab = SC[s2 * 64 + cc]; if (s2 < sg) hcur = ab.x * hcur + ab.y; }
;             float ysq[8];
; #pragma unroll
;             for (int i = 0; i < 8; ++i) { hcur = a8[i] * hcur + b8[i]; const float x = bf2f(ycur[i]);
;                 const float u2 = 1.5957691216f * (x + 0.044715f * x * x * x);
;                 const float y = hcur * (x * __builtin_amdgcn_rcpf(1.0f + __builtin_amdgcn_exp2f(-LOG2E * u2))); outp[((size_t)t0 + i) * DM] = (bf16)(cvtpk(y, 0.f) & 0xffffu); ysq[i] = y * y; }
	v_add_u32_e32 v82, 0x8400, v156
	v_add_u32_e32 v83, 0xc800, v156
	ds_read2_b32 v[124:125], v82 offset1:68
	ds_read2_b32 v[96:97], v83 offset1:68
	ds_read2_b32 v[94:95], v82 offset0:136 offset1:204
	ds_read2_b32 v[92:93], v83 offset0:136 offset1:204
	v_add_u32_e32 v83, 0x8800, v156
	v_add_u32_e32 v178, 0xcc00, v156
	ds_read2_b32 v[88:89], v83 offset0:16 offset1:84
	ds_read2_b32 v[86:87], v178 offset0:16 offset1:84
	s_waitcnt lgkmcnt(4)
	v_fma_f32 v84, 0, v124, v96
	v_fma_f32 v84, v84, v125, v97
	s_waitcnt lgkmcnt(2)
	v_fma_f32 v82, v84, v94, v92
	v_fma_f32 v82, v82, v95, v93
	s_waitcnt lgkmcnt(0)
	v_fma_f32 v91, v82, v88, v86
	ds_read2_b32 v[84:85], v83 offset0:152 offset1:220
	ds_read2_b32 v[82:83], v178 offset0:152 offset1:220
	v_mul_f32_e32 v90, v124, v125
	v_mov_b32_e32 v178, v94
	v_mov_b32_e32 v179, v89
	v_mov_b32_e32 v180, v95
	v_mov_b32_e32 v181, v87
	v_mul_f32_e32 v182, v90, v94
	v_pk_fma_f32 v[90:91], v[90:91], v[178:179], v[180:181]
	v_mul_f32_e32 v182, v182, v95
	v_mov_b32_e32 v183, v91
	v_mov_b32_e32 v90, v88
	s_waitcnt lgkmcnt(1)
	v_mov_b32_e32 v91, v84
	v_pk_mul_f32 v[178:179], v[182:183], v[90:91]
	v_mov_b32_e32 v180, v89
	v_mov_b32_e32 v184, v89
	s_waitcnt lgkmcnt(0)
	v_mov_b32_e32 v185, v82
	v_pk_mul_f32 v[178:179], v[178:179], v[180:181]
	v_pk_fma_f32 v[90:91], v[182:183], v[90:91], v[184:185]
	v_mov_b32_e32 v180, v85
	v_mov_b32_e32 v90, v178
	v_pk_mul_f32 v[178:179], v[178:179], v[84:85]
	v_mov_b32_e32 v182, v85
	v_mov_b32_e32 v183, v83
	v_pk_mul_f32 v[178:179], v[178:179], v[180:181]
	v_pk_fma_f32 v[90:91], v[90:91], v[84:85], v[182:183]
	s_nop 0
	v_mov_b32_e32 v179, v91
	ds_write_b64 v149, v[178:179]
	s_waitcnt lgkmcnt(0)
	s_barrier
	ds_read_b32 v90, v131
	ds_read_b64 v[214:215], v129
	ds_read_b64 v[216:217], v129 offset:512
	ds_read_b64 v[218:219], v129 offset:1024
	ds_read_b64 v[220:221], v129 offset:1536
	ds_read_b64 v[222:223], v129 offset:2048
	ds_read_b64 v[224:225], v129 offset:2560
	ds_read_b64 v[226:227], v129 offset:3072
	s_waitcnt lgkmcnt(6)
	v_fmac_f32_e32 v215, v90, v214
	v_cndmask_b32_e64 v90, v215, v90, s[4:5]
	s_waitcnt lgkmcnt(5)
	v_fmac_f32_e32 v217, v90, v216
	v_cndmask_b32_e64 v90, v90, v217, s[50:51]
	s_waitcnt lgkmcnt(4)
	v_fmac_f32_e32 v219, v90, v218
	v_cndmask_b32_e64 v90, v90, v219, s[54:55]
	s_waitcnt lgkmcnt(3)
	v_fmac_f32_e32 v221, v90, v220
	v_cndmask_b32_e64 v90, v90, v221, s[60:61]
	s_waitcnt lgkmcnt(2)
	v_fmac_f32_e32 v223, v90, v222
	v_cndmask_b32_e64 v90, v90, v223, s[62:63]
	s_waitcnt lgkmcnt(1)
	v_fmac_f32_e32 v225, v90, v224
	v_cndmask_b32_e64 v90, v90, v225, s[64:65]
	s_waitcnt lgkmcnt(0)
	v_fmac_f32_e32 v227, v90, v226
	v_cndmask_b32_e64 v90, v90, v227, s[66:67]
	s_waitcnt lgkmcnt(0)
	v_fma_f32 v96, v124, v90, v96
	v_lshlrev_b32_e32 v90, 16, v177
	v_mul_f32_e32 v91, 0x3d372713, v90
	v_mul_f32_e32 v91, v91, v90
	v_fma_f32 v91, v91, v90, v90
	v_mul_f32_e32 v91, 0x3fcc422a, v91
	v_mul_f32_e32 v91, 0xbfb8aa3b, v91
	v_exp_f32_e32 v91, v91
	v_fmac_f32_e32 v97, v125, v96
	s_mov_b32 s70, 0x9c001000
	v_fma_f32 v92, v94, v97, v92
	v_add_f32_e32 v91, 1.0, v91
	v_rcp_f32_e32 v91, v91
	v_lshlrev_b32_e32 v94, 16, v171
	v_fmac_f32_e32 v93, v95, v92
	v_fma_f32 v86, v88, v93, v86
	v_mul_f32_e32 v90, v91, v90
	v_mul_f32_e32 v177, v90, v96
	v_lshl_add_u64 v[90:91], s[22:23], 0, v[122:123]
	v_add_co_u32_e32 v178, vcc, 0x9c000000, v90
	v_cvt_pk_bf16_f32 v124, v177, s0
	s_nop 0
	v_addc_co_u32_e32 v179, vcc, 0, v91, vcc
	v_lshlrev_b32_e32 v96, 16, v176
	global_store_short v[178:179], v124, off offset:2048
	v_mul_f32_e32 v124, 0x3d372713, v96
	v_mul_f32_e32 v124, v124, v96
	v_fma_f32 v124, v124, v96, v96
	v_mul_f32_e32 v124, 0x3fcc422a, v124
	v_mul_f32_e32 v124, 0xbfb8aa3b, v124
	v_exp_f32_e32 v124, v124
	v_lshlrev_b32_e32 v88, 16, v165
	v_fmac_f32_e32 v87, v89, v86
	v_fma_f32 v82, v84, v87, v82
	v_add_f32_e32 v124, 1.0, v124
	v_rcp_f32_e32 v124, v124
	v_lshlrev_b32_e32 v84, 16, v163
	v_fmac_f32_e32 v83, v85, v82
	v_mul_f32_e32 v178, v177, v177
	v_mul_f32_e32 v96, v124, v96
	v_mul_f32_e32 v176, v96, v97
	v_add_co_u32_e32 v124, vcc, s70, v90
	v_cvt_pk_bf16_f32 v96, v176, s0
	s_nop 0
	v_addc_co_u32_e32 v125, vcc, 0, v91, vcc
	global_store_short v[124:125], v96, off offset:2048
	v_mul_f32_e32 v96, 0x3d372713, v94
	v_mul_f32_e32 v96, v96, v94
	v_fma_f32 v96, v96, v94, v94
	v_mul_f32_e32 v96, 0x3fcc422a, v96
	v_mul_f32_e32 v96, 0xbfb8aa3b, v96
	v_exp_f32_e32 v96, v96
	s_mov_b32 s70, 0x9c002000
	v_mul_f32_e32 v124, v176, v176
	v_add_f32_e32 v96, 1.0, v96
	v_rcp_f32_e32 v96, v96
	s_nop 0
	v_mul_f32_e32 v94, v96, v94
	v_mul_f32_e32 v125, v94, v92
	v_add_co_u32_e32 v96, vcc, s70, v90
	v_cvt_pk_bf16_f32 v94, v125, s0
	s_nop 0
	v_addc_co_u32_e32 v97, vcc, 0, v91, vcc
	v_lshlrev_b32_e32 v92, 16, v166
	global_store_short v[96:97], v94, off offset:2048
	v_mul_f32_e32 v94, 0x3d372713, v92
	v_mul_f32_e32 v94, v94, v92
	v_fma_f32 v94, v94, v92, v92
	v_mul_f32_e32 v94, 0x3fcc422a, v94
	v_mul_f32_e32 v94, 0xbfb8aa3b, v94
	v_exp_f32_e32 v94, v94
	s_mov_b32 s70, 0x9c003000
	v_mul_f32_e32 v96, v125, v125
	v_add_f32_e32 v94, 1.0, v94
	v_rcp_f32_e32 v94, v94
	s_nop 0
	v_mul_f32_e32 v92, v94, v92
	v_mul_f32_e32 v97, v92, v93
	v_add_co_u32_e32 v94, vcc, s70, v90
	v_cvt_pk_bf16_f32 v92, v97, s0
	s_nop 0
	v_addc_co_u32_e32 v95, vcc, 0, v91, vcc
	global_store_short v[94:95], v92, off offset:2048
	v_mul_f32_e32 v92, 0x3d372713, v88
	v_mul_f32_e32 v92, v92, v88
	v_fma_f32 v92, v92, v88, v88
	v_mul_f32_e32 v92, 0x3fcc422a, v92
	v_mul_f32_e32 v92, 0xbfb8aa3b, v92
	v_exp_f32_e32 v92, v92
	s_mov_b32 s70, 0x9c004000
	v_mul_f32_e32 v94, v97, v97
	v_add_f32_e32 v92, 1.0, v92
	v_rcp_f32_e32 v92, v92
	s_nop 0
	v_mul_f32_e32 v88, v92, v88
; __device__ __forceinline__ float bf2f(bf16 b) { return __uint_as_float(((unsigned)b) << 16); }
; __device__ __forceinline__ unsigned cvtpk(float lo, float hi) { const f32x2 v = {lo, hi}; return __builtin_bit_cast(unsigned, __builtin_convertvector(v, bf16x2_t)); }
; __device__ __forceinline__ void unit(LAS unsigned char* lds, const bf16* __restrict__ xr, const bf16* __restrict__ yg, const float* __restrict__ conv_w, const float* __restrict__ conv_b, const bf16* __restrict__ wga_t, const bf16* __restrict__ wgx_t, ...
;     ...
;             for (int i = 0; i < 8; ++i) { hcur = a8[i] * hcur + b8[i]; const float x = bf2f(ycur[i]);
;                 const float u2 = 1.5957691216f * (x + 0.044715f * x * x * x);
;                 const float y = hcur * (x * __builtin_amdgcn_rcpf(1.0f + __builtin_amdgcn_exp2f(-LOG2E * u2))); outp[((size_t)t0 + i) * DM] = (bf16)(cvtpk(y, 0.f) & 0xffffu); ysq[i] = y * y; }
; #pragma unroll
;             for (int i = 0; i < 8; ++i) { float v = ysq[i];
;                 v += __builtin_bit_cast(float, __builtin_amdgcn_update_dpp(0, __builtin_bit_cast(int, v), 0xB1, 0xf, 0xf, true));
;                 v += __builtin_bit_cast(float, __builtin_amdgcn_update_dpp(0, __builtin_bit_cast(int, v), 0x4E, 0xf, 0xf, true));
;                 v += __builtin_bit_cast(float, __builtin_amdgcn_update_dpp(0, __builtin_bit_cast(int, v), 0x141, 0xf, 0xf, true));
;                 v += __builtin_bit_cast(float, __builtin_amdgcn_update_dpp(0, __builtin_bit_cast(int, v), 0x140, 0xf, 0xf, true));
;                 v += __builtin_bit_cast(float, __builtin_amdgcn_update_dpp(0, __builtin_bit_cast(int, v), 0x142, 0xa, 0xf, false));
;                 v += __builtin_bit_cast(float, __builtin_amdgcn_update_dpp(0, __builtin_bit_cast(int, v), 0x143, 0xc, 0xf, false));
;                 ysq[i] = v; }
	v_mul_f32_e32 v95, v88, v86
	v_add_co_u32_e32 v92, vcc, s70, v90
	v_cvt_pk_bf16_f32 v88, v95, s0
	s_nop 0
	v_addc_co_u32_e32 v93, vcc, 0, v91, vcc
	v_lshlrev_b32_e32 v86, 16, v164
	global_store_short v[92:93], v88, off offset:2048
	v_mul_f32_e32 v88, 0x3d372713, v86
	v_mul_f32_e32 v88, v88, v86
	v_fma_f32 v88, v88, v86, v86
	v_mul_f32_e32 v88, 0x3fcc422a, v88
	v_mul_f32_e32 v88, 0xbfb8aa3b, v88
	v_exp_f32_e32 v88, v88
	s_mov_b32 s70, 0x9c005000
	v_mul_f32_e32 v92, v95, v95
	v_add_f32_e32 v88, 1.0, v88
	v_rcp_f32_e32 v88, v88
	s_nop 0
	v_mul_f32_e32 v86, v88, v86
	v_mul_f32_e32 v93, v86, v87
	v_add_co_u32_e32 v88, vcc, s70, v90
	v_cvt_pk_bf16_f32 v86, v93, s0
	s_nop 0
	v_addc_co_u32_e32 v89, vcc, 0, v91, vcc
	global_store_short v[88:89], v86, off offset:2048
	v_mul_f32_e32 v86, 0x3d372713, v84
	v_mul_f32_e32 v86, v86, v84
	v_fma_f32 v86, v86, v84, v84
	v_mul_f32_e32 v86, 0x3fcc422a, v86
	v_mul_f32_e32 v86, 0xbfb8aa3b, v86
	v_exp_f32_e32 v86, v86
	s_mov_b32 s70, 0x9c006000
	v_mul_f32_e32 v164, v93, v93
	v_mov_b32_dpp v89, v94 quad_perm:[1,0,3,2] row_mask:0xf bank_mask:0xf bound_ctrl:1
	v_add_f32_e32 v86, 1.0, v86
	v_rcp_f32_e32 v86, v86
	v_fmac_f32_e32 v89, v97, v97
	v_mov_b32_dpp v94, v164 quad_perm:[1,0,3,2] row_mask:0xf bank_mask:0xf bound_ctrl:1
	v_fmac_f32_e32 v94, v93, v93
	v_mul_f32_e32 v84, v86, v84
	v_mul_f32_e32 v163, v84, v82
	v_add_co_u32_e32 v86, vcc, s70, v90
	v_cvt_pk_bf16_f32 v84, v163, s0
	s_nop 0
	v_addc_co_u32_e32 v87, vcc, 0, v91, vcc
	v_lshlrev_b32_e32 v82, 16, v162
	global_store_short v[86:87], v84, off offset:2048
	v_mul_f32_e32 v84, 0x3d372713, v82
	v_mul_f32_e32 v84, v84, v82
	v_fma_f32 v84, v84, v82, v82
	v_mul_f32_e32 v84, 0x3fcc422a, v84
	v_mul_f32_e32 v84, 0xbfb8aa3b, v84
	v_exp_f32_e32 v84, v84
	s_mov_b32 s70, 0x9c007000
	v_mul_f32_e32 v165, v163, v163
	v_mov_b32_dpp v87, v96 quad_perm:[1,0,3,2] row_mask:0xf bank_mask:0xf bound_ctrl:1
	v_add_f32_e32 v84, 1.0, v84
	v_rcp_f32_e32 v84, v84
	v_fmac_f32_e32 v87, v125, v125
	v_add_f32_dpp v89, v89, v89 quad_perm:[2,3,0,1] row_mask:0xf bank_mask:0xf bound_ctrl:1
	v_add_f32_dpp v93, v94, v94 quad_perm:[2,3,0,1] row_mask:0xf bank_mask:0xf bound_ctrl:1
	v_mul_f32_e32 v82, v84, v82
	v_mul_f32_e32 v162, v82, v83
	v_add_co_u32_e32 v84, vcc, s70, v90
	v_cvt_pk_bf16_f32 v82, v162, s0
	s_nop 0
	v_addc_co_u32_e32 v85, vcc, 0, v91, vcc
	v_mul_f32_e32 v166, v162, v162
	v_mov_b32_dpp v91, v92 quad_perm:[1,0,3,2] row_mask:0xf bank_mask:0xf bound_ctrl:1
	global_store_short v[84:85], v82, off offset:2048
	v_mov_b32_dpp v82, v178 quad_perm:[1,0,3,2] row_mask:0xf bank_mask:0xf bound_ctrl:1
	v_mov_b32_dpp v85, v124 quad_perm:[1,0,3,2] row_mask:0xf bank_mask:0xf bound_ctrl:1
	v_fmac_f32_e32 v91, v95, v95
	v_mov_b32_dpp v95, v165 quad_perm:[1,0,3,2] row_mask:0xf bank_mask:0xf bound_ctrl:1
	v_mov_b32_dpp v97, v166 quad_perm:[1,0,3,2] row_mask:0xf bank_mask:0xf bound_ctrl:1
	v_fmac_f32_e32 v82, v177, v177
	v_fmac_f32_e32 v85, v176, v176
	v_fmac_f32_e32 v95, v163, v163
	v_fmac_f32_e32 v97, v162, v162
	v_add_f32_dpp v82, v82, v82 quad_perm:[2,3,0,1] row_mask:0xf bank_mask:0xf bound_ctrl:1
	v_add_f32_dpp v85, v85, v85 quad_perm:[2,3,0,1] row_mask:0xf bank_mask:0xf bound_ctrl:1
	v_add_f32_dpp v87, v87, v87 quad_perm:[2,3,0,1] row_mask:0xf bank_mask:0xf bound_ctrl:1
	v_add_f32_dpp v91, v91, v91 quad_perm:[2,3,0,1] row_mask:0xf bank_mask:0xf bound_ctrl:1
	v_add_f32_dpp v95, v95, v95 quad_perm:[2,3,0,1] row_mask:0xf bank_mask:0xf bound_ctrl:1
	v_add_f32_dpp v97, v97, v97 quad_perm:[2,3,0,1] row_mask:0xf bank_mask:0xf bound_ctrl:1
	v_add_f32_dpp v82, v82, v82 row_half_mirror row_mask:0xf bank_mask:0xf bound_ctrl:1
	v_add_f32_dpp v85, v85, v85 row_half_mirror row_mask:0xf bank_mask:0xf bound_ctrl:1
	v_add_f32_dpp v87, v87, v87 row_half_mirror row_mask:0xf bank_mask:0xf bound_ctrl:1
	v_add_f32_dpp v89, v89, v89 row_half_mirror row_mask:0xf bank_mask:0xf bound_ctrl:1
	v_add_f32_dpp v91, v91, v91 row_half_mirror row_mask:0xf bank_mask:0xf bound_ctrl:1
	v_add_f32_dpp v93, v93, v93 row_half_mirror row_mask:0xf bank_mask:0xf bound_ctrl:1
	v_add_f32_dpp v95, v95, v95 row_half_mirror row_mask:0xf bank_mask:0xf bound_ctrl:1
	v_add_f32_dpp v97, v97, v97 row_half_mirror row_mask:0xf bank_mask:0xf bound_ctrl:1
	v_add_f32_dpp v82, v82, v82 row_mirror row_mask:0xf bank_mask:0xf bound_ctrl:1
	v_mov_b32_e32 v84, 0
	v_add_f32_dpp v85, v85, v85 row_mirror row_mask:0xf bank_mask:0xf bound_ctrl:1
	v_mov_b32_e32 v86, 0
	v_add_f32_dpp v87, v87, v87 row_mirror row_mask:0xf bank_mask:0xf bound_ctrl:1
	v_mov_b32_e32 v88, 0
	v_add_f32_dpp v89, v89, v89 row_mirror row_mask:0xf bank_mask:0xf bound_ctrl:1
	v_mov_b32_e32 v90, 0
	v_add_f32_dpp v91, v91, v91 row_mirror row_mask:0xf bank_mask:0xf bound_ctrl:1
	v_mov_b32_e32 v92, 0
	v_add_f32_dpp v93, v93, v93 row_mirror row_mask:0xf bank_mask:0xf bound_ctrl:1
	v_mov_b32_e32 v94, 0
	v_add_f32_dpp v95, v95, v95 row_mirror row_mask:0xf bank_mask:0xf bound_ctrl:1
	v_mov_b32_e32 v96, 0
	v_add_f32_dpp v97, v97, v97 row_mirror row_mask:0xf bank_mask:0xf bound_ctrl:1
	v_mov_b32_e32 v124, 0
	v_mov_b32_dpp v84, v82 row_bcast:15 row_mask:0xa bank_mask:0xf
	v_mov_b32_dpp v86, v85 row_bcast:15 row_mask:0xa bank_mask:0xf
	v_mov_b32_dpp v88, v87 row_bcast:15 row_mask:0xa bank_mask:0xf
	v_mov_b32_dpp v90, v89 row_bcast:15 row_mask:0xa bank_mask:0xf
	v_mov_b32_dpp v92, v91 row_bcast:15 row_mask:0xa bank_mask:0xf
	v_mov_b32_dpp v94, v93 row_bcast:15 row_mask:0xa bank_mask:0xf
	v_mov_b32_dpp v96, v95 row_bcast:15 row_mask:0xa bank_mask:0xf
	v_mov_b32_dpp v124, v97 row_bcast:15 row_mask:0xa bank_mask:0xf
	v_add_f32_e32 v82, v82, v84
	v_mov_b32_e32 v84, 0
	v_add_f32_e32 v85, v85, v86
	v_mov_b32_e32 v86, 0
	v_add_f32_e32 v87, v87, v88
	v_mov_b32_e32 v88, 0
	v_add_f32_e32 v89, v89, v90
	v_mov_b32_e32 v90, 0
	v_add_f32_e32 v91, v91, v92
	v_mov_b32_e32 v92, 0
	v_add_f32_e32 v93, v93, v94
	v_mov_b32_e32 v94, 0
	v_add_f32_e32 v95, v95, v96
	v_mov_b32_e32 v96, 0
	v_add_f32_e32 v97, v97, v124
	v_mov_b32_e32 v124, 0
	v_mov_b32_dpp v84, v82 row_bcast:31 row_mask:0xc bank_mask:0xf
	v_mov_b32_dpp v86, v85 row_bcast:31 row_mask:0xc bank_mask:0xf
	v_mov_b32_dpp v88, v87 row_bcast:31 row_mask:0xc bank_mask:0xf
	v_mov_b32_dpp v90, v89 row_bcast:31 row_mask:0xc bank_mask:0xf
	v_mov_b32_dpp v92, v91 row_bcast:31 row_mask:0xc bank_mask:0xf
	v_mov_b32_dpp v94, v93 row_bcast:31 row_mask:0xc bank_mask:0xf
	v_mov_b32_dpp v96, v95 row_bcast:31 row_mask:0xc bank_mask:0xf
	v_mov_b32_dpp v124, v97 row_bcast:31 row_mask:0xc bank_mask:0xf
	s_and_saveexec_b64 s[70:71], s[8:9]
	s_cbranch_execz .LBB5_965
; __device__ __forceinline__ void unit(LAS unsigned char* lds, const bf16* __restrict__ xr, const bf16* __restrict__ yg, const float* __restrict__ conv_w, const float* __restrict__ conv_b, const bf16* __restrict__ wga_t, const bf16* __restrict__ wgx_t, ...
;     ...
;             if (lane == 63) {
; #pragma unroll
;                 for (int i = 0; i < 8; ++i) ssl[((size_t)b * SEQ + t0 + 8 * sg + i) * 16 + g] = ysq[i]; }
	s_add_u32 s92, s22, s34
	v_add_f32_e32 v82, v82, v84
	s_addc_u32 s93, s23, s89
	v_add_f32_e32 v97, v97, v124
	v_add_f32_e32 v95, v95, v96
	v_add_f32_e32 v93, v93, v94
	v_add_f32_e32 v91, v91, v92
	v_add_f32_e32 v89, v89, v90
	v_add_f32_e32 v87, v87, v88
	v_add_f32_e32 v85, v85, v86
	global_store_dword v99, v82, s[92:93] offset:-256
	global_store_dword v99, v85, s[92:93] offset:-192
	global_store_dword v99, v87, s[92:93] offset:-128
	global_store_dword v99, v89, s[92:93] offset:-64
	global_store_dword v99, v91, s[92:93]
	global_store_dword v99, v93, s[92:93] offset:64
	global_store_dword v99, v95, s[92:93] offset:128
	global_store_dword v99, v97, s[92:93] offset:192
